# speedup vs baseline: 1.0016x; 1.0016x over previous
.LBB5_140:
	v_readfirstlane_b32 s98, v0
	s_bfe_u32 s98, s98, 0x10008
	v_lshl_or_b32 v2, s42, 3, v187
	v_ashrrev_i32_e32 v3, 31, v2
	v_lshlrev_b64 v[2:3], 16, v[2:3]
	v_lshl_add_u64 v[2:3], s[48:49], 0, v[2:3]
	v_mov_b32_e32 v169, 0
	v_lshlrev_b32_e32 v168, 4, v189
	s_or_b32 s25, s2, s50
	s_or_b32 s24, s50, 1
	s_mov_b32 s1, 0
	v_lshl_add_u64 v[166:167], v[2:3], 0, v[168:169]
	s_lshl_b32 s0, s25, 12
	s_or_b32 s30, s2, s24
	v_lshl_add_u64 v[18:19], v[166:167], 0, s[0:1]
	s_lshl_b32 s0, s30, 12
	v_lshl_add_u64 v[34:35], v[166:167], 0, s[0:1]
	s_waitcnt vmcnt(8)
	v_mov_b32_e32 v2, v200
	v_mov_b32_e32 v3, v201
	v_mov_b32_e32 v4, v202
	v_mov_b32_e32 v5, v203
	v_mov_b32_e32 v6, v204
	v_mov_b32_e32 v7, v205
	v_mov_b32_e32 v8, v206
	v_mov_b32_e32 v9, v207
	v_mov_b32_e32 v10, v208
	v_mov_b32_e32 v11, v209
	v_mov_b32_e32 v12, v210
	v_mov_b32_e32 v13, v211
	v_mov_b32_e32 v14, v212
	v_mov_b32_e32 v15, v213
	v_mov_b32_e32 v16, v214
	v_mov_b32_e32 v17, v215
	v_mov_b32_e32 v18, v216
	v_mov_b32_e32 v19, v217
	v_mov_b32_e32 v20, v218
	v_mov_b32_e32 v21, v219
	v_mov_b32_e32 v22, v220
	v_mov_b32_e32 v23, v221
	v_mov_b32_e32 v24, v222
	v_mov_b32_e32 v25, v223
	v_mov_b32_e32 v26, v224
	v_mov_b32_e32 v27, v225
	v_mov_b32_e32 v28, v226
	v_mov_b32_e32 v29, v227
	v_mov_b32_e32 v30, v228
	v_mov_b32_e32 v31, v229
	v_mov_b32_e32 v32, v230
	v_mov_b32_e32 v33, v231
	v_or_b32_e32 v52, v147, v146
	s_add_i32 s0, s59, 2
	s_and_b32 s28, s0, 6
	s_or_b32 s31, s2, s28
	s_lshl_b32 s0, s31, 12
	v_lshl_add_u64 v[50:51], v[166:167], 0, s[0:1]
	s_waitcnt lgkmcnt(0)
	s_barrier
	global_load_dwordx4 v[34:37], v[50:51], off
	global_load_dwordx4 v[38:41], v[50:51], off offset:1024
	global_load_dwordx4 v[42:45], v[50:51], off offset:2048
	global_load_dwordx4 v[46:49], v[50:51], off offset:3072
	s_cmp_eq_u32 s98, 0
	s_cbranch_scc1 .Lstag_1
	s_sleep 4
.Lstag_1:
	v_xad_u32 v191, v52, v152, 0
	v_lshl_add_u32 v122, s25, 10, v191
	ds_read_b128 v[50:53], v122
	ds_read_b128 v[54:57], v122 offset:16384
	ds_read_b128 v[58:61], v122 offset:32768
	ds_read_b128 v[62:65], v122 offset:49152
	s_setprio 1
	s_waitcnt vmcnt(19) lgkmcnt(3)
	v_mfma_f32_16x16x32_f16 v[66:69], v[2:5], v[50:53], 0
	s_waitcnt vmcnt(18)
	v_mfma_f32_16x16x32_f16 v[70:73], v[6:9], v[50:53], 0
	s_waitcnt vmcnt(17)
	v_mfma_f32_16x16x32_f16 v[74:77], v[10:13], v[50:53], 0
	s_waitcnt vmcnt(16)
	v_mfma_f32_16x16x32_f16 v[50:53], v[14:17], v[50:53], 0
	s_waitcnt lgkmcnt(2)
	v_mfma_f32_16x16x32_f16 v[78:81], v[2:5], v[54:57], 0
	v_mfma_f32_16x16x32_f16 v[82:85], v[6:9], v[54:57], 0
	v_mfma_f32_16x16x32_f16 v[86:89], v[10:13], v[54:57], 0
	v_mfma_f32_16x16x32_f16 v[54:57], v[14:17], v[54:57], 0
	s_waitcnt lgkmcnt(1)
	v_mfma_f32_16x16x32_f16 v[90:93], v[2:5], v[58:61], 0
	v_mfma_f32_16x16x32_f16 v[94:97], v[6:9], v[58:61], 0
	v_mfma_f32_16x16x32_f16 v[98:101], v[10:13], v[58:61], 0
	v_mfma_f32_16x16x32_f16 v[58:61], v[14:17], v[58:61], 0
	s_waitcnt lgkmcnt(0)
	v_mfma_f32_16x16x32_f16 v[102:105], v[2:5], v[62:65], 0
	v_mfma_f32_16x16x32_f16 v[106:109], v[6:9], v[62:65], 0
	v_mfma_f32_16x16x32_f16 v[110:113], v[10:13], v[62:65], 0
	v_mfma_f32_16x16x32_f16 v[62:65], v[14:17], v[62:65], 0
	s_setprio 0
	v_add_u32_e32 v114, 0x10000, v122
	v_add_u32_e32 v118, 0x14000, v122
	v_add_u32_e32 v123, 0x18000, v122
	v_add_u32_e32 v126, 0x1c000, v122
	ds_read_b128 v[114:117], v114
	ds_read_b128 v[118:121], v118
	ds_read_b128 v[122:125], v123
	ds_read_b128 v[126:129], v126
	s_setprio 1
	s_waitcnt lgkmcnt(3)
	v_mfma_f32_16x16x32_f16 v[130:133], v[2:5], v[114:117], 0
	v_mfma_f32_16x16x32_f16 v[134:137], v[6:9], v[114:117], 0
	v_mfma_f32_16x16x32_f16 v[138:141], v[10:13], v[114:117], 0
	v_mfma_f32_16x16x32_f16 v[114:117], v[14:17], v[114:117], 0
	s_waitcnt lgkmcnt(2)
	v_mfma_f32_16x16x32_f16 v[142:145], v[2:5], v[118:121], 0
	v_mfma_f32_16x16x32_f16 v[146:149], v[6:9], v[118:121], 0
	v_mfma_f32_16x16x32_f16 v[150:153], v[10:13], v[118:121], 0
	v_mfma_f32_16x16x32_f16 v[118:121], v[14:17], v[118:121], 0
	s_waitcnt lgkmcnt(1)
	v_mfma_f32_16x16x32_f16 v[154:157], v[2:5], v[122:125], 0
	v_mfma_f32_16x16x32_f16 v[158:161], v[6:9], v[122:125], 0
	v_mfma_f32_16x16x32_f16 v[170:173], v[10:13], v[122:125], 0
	v_mfma_f32_16x16x32_f16 v[122:125], v[14:17], v[122:125], 0
	s_waitcnt lgkmcnt(0)
	v_mfma_f32_16x16x32_f16 v[2:5], v[2:5], v[126:129], 0
	v_mfma_f32_16x16x32_f16 v[6:9], v[6:9], v[126:129], 0
	v_mfma_f32_16x16x32_f16 v[10:13], v[10:13], v[126:129], 0
	v_mfma_f32_16x16x32_f16 v[14:17], v[14:17], v[126:129], 0
	s_setprio 0
	s_add_i32 s0, s50, 3
	s_and_b32 s29, s0, 7
	s_or_b32 s48, s29, s2
	s_lshl_b32 s0, s48, 12
	v_lshl_add_u64 v[178:179], v[166:167], 0, s[0:1]
	global_load_dwordx4 v[126:129], v[178:179], off
	global_load_dwordx4 v[174:177], v[178:179], off offset:1024
	global_load_dwordx4 v[192:195], v[178:179], off offset:2048
	global_load_dwordx4 v[196:199], v[178:179], off offset:3072
	v_lshl_add_u32 v163, s30, 10, v191
	ds_read_b128 v[200:203], v163
	ds_read_b128 v[204:207], v163 offset:16384
	ds_read_b128 v[208:211], v163 offset:32768
	ds_read_b128 v[212:215], v163 offset:49152
	s_setprio 1
	s_waitcnt vmcnt(19) lgkmcnt(3)
	v_mfma_f32_16x16x32_f16 v[66:69], v[18:21], v[200:203], v[66:69]
	s_waitcnt vmcnt(18)
	v_mfma_f32_16x16x32_f16 v[70:73], v[22:25], v[200:203], v[70:73]
	s_waitcnt vmcnt(17)
	v_mfma_f32_16x16x32_f16 v[74:77], v[26:29], v[200:203], v[74:77]
	s_waitcnt vmcnt(16)
	v_mfma_f32_16x16x32_f16 v[50:53], v[30:33], v[200:203], v[50:53]
	s_waitcnt lgkmcnt(2)
	v_mfma_f32_16x16x32_f16 v[78:81], v[18:21], v[204:207], v[78:81]
	v_mfma_f32_16x16x32_f16 v[82:85], v[22:25], v[204:207], v[82:85]
	v_mfma_f32_16x16x32_f16 v[86:89], v[26:29], v[204:207], v[86:89]
	v_mfma_f32_16x16x32_f16 v[54:57], v[30:33], v[204:207], v[54:57]
	s_waitcnt lgkmcnt(1)
	v_mfma_f32_16x16x32_f16 v[90:93], v[18:21], v[208:211], v[90:93]
	v_mfma_f32_16x16x32_f16 v[94:97], v[22:25], v[208:211], v[94:97]
	v_mfma_f32_16x16x32_f16 v[98:101], v[26:29], v[208:211], v[98:101]
	v_mfma_f32_16x16x32_f16 v[58:61], v[30:33], v[208:211], v[58:61]
	s_waitcnt lgkmcnt(0)
	v_mfma_f32_16x16x32_f16 v[102:105], v[18:21], v[212:215], v[102:105]
	v_mfma_f32_16x16x32_f16 v[106:109], v[22:25], v[212:215], v[106:109]
	v_mfma_f32_16x16x32_f16 v[110:113], v[26:29], v[212:215], v[110:113]
	v_mfma_f32_16x16x32_f16 v[62:65], v[30:33], v[212:215], v[62:65]
	s_setprio 0
	v_add_u32_e32 v165, 0x10000, v163
	v_add_u32_e32 v168, 0x14000, v163
	ds_read_b128 v[200:203], v165
	ds_read_b128 v[204:207], v168
	v_add_u32_e32 v165, 0x18000, v163
	v_add_u32_e32 v163, 0x1c000, v163
	ds_read_b128 v[208:211], v165
	ds_read_b128 v[212:215], v163
	s_setprio 1
	s_waitcnt lgkmcnt(3)
	v_mfma_f32_16x16x32_f16 v[130:133], v[18:21], v[200:203], v[130:133]
	v_mfma_f32_16x16x32_f16 v[134:137], v[22:25], v[200:203], v[134:137]
	v_mfma_f32_16x16x32_f16 v[138:141], v[26:29], v[200:203], v[138:141]
	v_mfma_f32_16x16x32_f16 v[114:117], v[30:33], v[200:203], v[114:117]
	s_waitcnt lgkmcnt(2)
	v_mfma_f32_16x16x32_f16 v[142:145], v[18:21], v[204:207], v[142:145]
	v_mfma_f32_16x16x32_f16 v[146:149], v[22:25], v[204:207], v[146:149]
	v_mfma_f32_16x16x32_f16 v[150:153], v[26:29], v[204:207], v[150:153]
	v_mfma_f32_16x16x32_f16 v[118:121], v[30:33], v[204:207], v[118:121]
	s_waitcnt lgkmcnt(1)
	v_mfma_f32_16x16x32_f16 v[154:157], v[18:21], v[208:211], v[154:157]
	v_mfma_f32_16x16x32_f16 v[158:161], v[22:25], v[208:211], v[158:161]
	v_mfma_f32_16x16x32_f16 v[122:125], v[30:33], v[208:211], v[122:125]
	s_waitcnt lgkmcnt(0)
	v_mfma_f32_16x16x32_f16 v[2:5], v[18:21], v[212:215], v[2:5]
	v_mfma_f32_16x16x32_f16 v[6:9], v[22:25], v[212:215], v[6:9]
	v_mfma_f32_16x16x32_f16 v[10:13], v[26:29], v[212:215], v[10:13]
	v_mfma_f32_16x16x32_f16 v[14:17], v[30:33], v[212:215], v[14:17]
	v_mfma_f32_16x16x32_f16 v[170:173], v[26:29], v[208:211], v[170:173]
	s_setprio 0
	s_xor_b32 s25, s25, 4
	s_lshl_b32 s0, s25, 12
	v_lshl_add_u64 v[30:31], v[166:167], 0, s[0:1]
	s_waitcnt vmcnt(8)
	s_barrier
	s_getreg_b32 s80, hwreg(HW_REG_XCC_ID, 0, 4)
	s_and_b32 s80, s80, 15
	s_add_i32 s80, s80, 1
	s_lshl_b32 s81, s34, 3
	s_or_b32 s81, s81, s33
	s_lshl_b32 s81, s81, 7
	s_add_u32 s82, s46, s81
	s_addc_u32 s83, s47, 0
	v_mov_b32_e32 v254, 0
	v_mov_b32_e32 v255, s80
	s_and_saveexec_b64 s[84:85], s[4:5]
	global_store_dword v254, v255, s[82:83] sc1
	s_mov_b64 exec, s[84:85]
	s_cmp_eq_u32 s98, 0
	s_cbranch_scc1 .Lstag_2
	s_sleep 4
.Lstag_2:
	global_load_dwordx4 v[18:21], v[30:31], off
	global_load_dwordx4 v[22:25], v[30:31], off offset:1024
	global_load_dwordx4 v[26:29], v[30:31], off offset:2048
	s_nop 0
	global_load_dwordx4 v[30:33], v[30:31], off offset:3072
	v_lshl_add_u32 v163, s31, 10, v191
	ds_read_b128 v[200:203], v163
	ds_read_b128 v[204:207], v163 offset:16384
	ds_read_b128 v[208:211], v163 offset:32768
	ds_read_b128 v[212:215], v163 offset:49152
	s_setprio 1
	s_waitcnt vmcnt(11) lgkmcnt(3)
	v_mfma_f32_16x16x32_f16 v[66:69], v[34:37], v[200:203], v[66:69]
	s_waitcnt vmcnt(10)
	v_mfma_f32_16x16x32_f16 v[70:73], v[38:41], v[200:203], v[70:73]
	s_waitcnt vmcnt(9)
	v_mfma_f32_16x16x32_f16 v[74:77], v[42:45], v[200:203], v[74:77]
	s_waitcnt vmcnt(8)
	v_mfma_f32_16x16x32_f16 v[50:53], v[46:49], v[200:203], v[50:53]
	s_waitcnt lgkmcnt(2)
	v_mfma_f32_16x16x32_f16 v[78:81], v[34:37], v[204:207], v[78:81]
	v_mfma_f32_16x16x32_f16 v[82:85], v[38:41], v[204:207], v[82:85]
	v_mfma_f32_16x16x32_f16 v[86:89], v[42:45], v[204:207], v[86:89]
	v_mfma_f32_16x16x32_f16 v[54:57], v[46:49], v[204:207], v[54:57]
	s_waitcnt lgkmcnt(1)
	v_mfma_f32_16x16x32_f16 v[90:93], v[34:37], v[208:211], v[90:93]
	v_mfma_f32_16x16x32_f16 v[94:97], v[38:41], v[208:211], v[94:97]
	v_mfma_f32_16x16x32_f16 v[98:101], v[42:45], v[208:211], v[98:101]
	v_mfma_f32_16x16x32_f16 v[58:61], v[46:49], v[208:211], v[58:61]
	s_waitcnt lgkmcnt(0)
	v_mfma_f32_16x16x32_f16 v[102:105], v[34:37], v[212:215], v[102:105]
	v_mfma_f32_16x16x32_f16 v[106:109], v[38:41], v[212:215], v[106:109]
	v_mfma_f32_16x16x32_f16 v[110:113], v[42:45], v[212:215], v[110:113]
	v_mfma_f32_16x16x32_f16 v[62:65], v[46:49], v[212:215], v[62:65]
	s_setprio 0
	v_add_u32_e32 v165, 0x10000, v163
	v_add_u32_e32 v168, 0x14000, v163
	ds_read_b128 v[200:203], v165
	ds_read_b128 v[204:207], v168
	v_add_u32_e32 v165, 0x18000, v163
	v_add_u32_e32 v163, 0x1c000, v163
	ds_read_b128 v[208:211], v165
	ds_read_b128 v[212:215], v163
	s_setprio 1
	s_waitcnt lgkmcnt(3)
	v_mfma_f32_16x16x32_f16 v[130:133], v[34:37], v[200:203], v[130:133]
	v_mfma_f32_16x16x32_f16 v[134:137], v[38:41], v[200:203], v[134:137]
	v_mfma_f32_16x16x32_f16 v[138:141], v[42:45], v[200:203], v[138:141]
	v_mfma_f32_16x16x32_f16 v[114:117], v[46:49], v[200:203], v[114:117]
	s_waitcnt lgkmcnt(2)
	v_mfma_f32_16x16x32_f16 v[142:145], v[34:37], v[204:207], v[142:145]
	v_mfma_f32_16x16x32_f16 v[146:149], v[38:41], v[204:207], v[146:149]
	v_mfma_f32_16x16x32_f16 v[150:153], v[42:45], v[204:207], v[150:153]
	v_mfma_f32_16x16x32_f16 v[118:121], v[46:49], v[204:207], v[118:121]
	s_waitcnt lgkmcnt(1)
	v_mfma_f32_16x16x32_f16 v[154:157], v[34:37], v[208:211], v[154:157]
	v_mfma_f32_16x16x32_f16 v[158:161], v[38:41], v[208:211], v[158:161]
	v_mfma_f32_16x16x32_f16 v[122:125], v[46:49], v[208:211], v[122:125]
	s_waitcnt lgkmcnt(0)
	v_mfma_f32_16x16x32_f16 v[2:5], v[34:37], v[212:215], v[2:5]
	v_mfma_f32_16x16x32_f16 v[6:9], v[38:41], v[212:215], v[6:9]
	v_mfma_f32_16x16x32_f16 v[10:13], v[42:45], v[212:215], v[10:13]
	v_mfma_f32_16x16x32_f16 v[14:17], v[46:49], v[212:215], v[14:17]
	v_mfma_f32_16x16x32_f16 v[170:173], v[42:45], v[208:211], v[170:173]
	s_setprio 0
	s_add_i32 s0, s50, 5
	s_and_b32 s30, s0, 7
	s_or_b32 s49, s30, s2
	s_lshl_b32 s0, s49, 12
	v_lshl_add_u64 v[46:47], v[166:167], 0, s[0:1]
	global_load_dwordx4 v[34:37], v[46:47], off
	global_load_dwordx4 v[38:41], v[46:47], off offset:1024
	global_load_dwordx4 v[42:45], v[46:47], off offset:2048
	s_nop 0
	global_load_dwordx4 v[46:49], v[46:47], off offset:3072
	v_lshl_add_u32 v163, s48, 10, v191
	ds_read_b128 v[200:203], v163
	ds_read_b128 v[204:207], v163 offset:16384
	ds_read_b128 v[208:211], v163 offset:32768
	ds_read_b128 v[212:215], v163 offset:49152
	s_setprio 1
	s_waitcnt vmcnt(11) lgkmcnt(3)
	v_mfma_f32_16x16x32_f16 v[66:69], v[126:129], v[200:203], v[66:69]
	s_waitcnt vmcnt(10)
	v_mfma_f32_16x16x32_f16 v[70:73], v[174:177], v[200:203], v[70:73]
	s_waitcnt vmcnt(9)
	v_mfma_f32_16x16x32_f16 v[74:77], v[192:195], v[200:203], v[74:77]
	s_waitcnt vmcnt(8)
	v_mfma_f32_16x16x32_f16 v[50:53], v[196:199], v[200:203], v[50:53]
	s_waitcnt lgkmcnt(2)
	v_mfma_f32_16x16x32_f16 v[78:81], v[126:129], v[204:207], v[78:81]
	v_mfma_f32_16x16x32_f16 v[82:85], v[174:177], v[204:207], v[82:85]
	v_mfma_f32_16x16x32_f16 v[86:89], v[192:195], v[204:207], v[86:89]
	v_mfma_f32_16x16x32_f16 v[54:57], v[196:199], v[204:207], v[54:57]
	s_waitcnt lgkmcnt(1)
	v_mfma_f32_16x16x32_f16 v[90:93], v[126:129], v[208:211], v[90:93]
	v_mfma_f32_16x16x32_f16 v[94:97], v[174:177], v[208:211], v[94:97]
	v_mfma_f32_16x16x32_f16 v[98:101], v[192:195], v[208:211], v[98:101]
	v_mfma_f32_16x16x32_f16 v[58:61], v[196:199], v[208:211], v[58:61]
	s_waitcnt lgkmcnt(0)
	v_mfma_f32_16x16x32_f16 v[102:105], v[126:129], v[212:215], v[102:105]
	v_mfma_f32_16x16x32_f16 v[106:109], v[174:177], v[212:215], v[106:109]
	v_mfma_f32_16x16x32_f16 v[110:113], v[192:195], v[212:215], v[110:113]
	v_mfma_f32_16x16x32_f16 v[62:65], v[196:199], v[212:215], v[62:65]
	s_setprio 0
	v_add_u32_e32 v165, 0x10000, v163
	v_add_u32_e32 v168, 0x14000, v163
	ds_read_b128 v[200:203], v165
	ds_read_b128 v[204:207], v168
	v_add_u32_e32 v165, 0x18000, v163
	v_add_u32_e32 v163, 0x1c000, v163
	ds_read_b128 v[208:211], v165
	ds_read_b128 v[212:215], v163
	s_setprio 1
	s_waitcnt lgkmcnt(3)
	v_mfma_f32_16x16x32_f16 v[130:133], v[126:129], v[200:203], v[130:133]
	v_mfma_f32_16x16x32_f16 v[134:137], v[174:177], v[200:203], v[134:137]
	v_mfma_f32_16x16x32_f16 v[138:141], v[192:195], v[200:203], v[138:141]
	v_mfma_f32_16x16x32_f16 v[114:117], v[196:199], v[200:203], v[114:117]
	s_waitcnt lgkmcnt(2)
	v_mfma_f32_16x16x32_f16 v[142:145], v[126:129], v[204:207], v[142:145]
	v_mfma_f32_16x16x32_f16 v[146:149], v[174:177], v[204:207], v[146:149]
	v_mfma_f32_16x16x32_f16 v[150:153], v[192:195], v[204:207], v[150:153]
	v_mfma_f32_16x16x32_f16 v[118:121], v[196:199], v[204:207], v[118:121]
	s_waitcnt lgkmcnt(1)
	v_mfma_f32_16x16x32_f16 v[154:157], v[126:129], v[208:211], v[154:157]
	v_mfma_f32_16x16x32_f16 v[158:161], v[174:177], v[208:211], v[158:161]
	v_mfma_f32_16x16x32_f16 v[122:125], v[196:199], v[208:211], v[122:125]
	s_waitcnt lgkmcnt(0)
	v_mfma_f32_16x16x32_f16 v[2:5], v[126:129], v[212:215], v[2:5]
	v_mfma_f32_16x16x32_f16 v[6:9], v[174:177], v[212:215], v[6:9]
	v_mfma_f32_16x16x32_f16 v[10:13], v[192:195], v[212:215], v[10:13]
	v_mfma_f32_16x16x32_f16 v[14:17], v[196:199], v[212:215], v[14:17]
	v_mfma_f32_16x16x32_f16 v[170:173], v[192:195], v[208:211], v[170:173]
	s_setprio 0
	s_add_i32 s59, s59, 6
	s_and_b32 s31, s59, 6
	s_or_b32 s52, s2, s31
	s_lshl_b32 s0, s52, 12
	v_lshl_add_u64 v[178:179], v[166:167], 0, s[0:1]
	s_lshl_b32 s86, s34, 3
	s_or_b32 s86, s86, s33
	s_xor_b32 s86, s86, 1
	s_lshl_b32 s86, s86, 7
	s_add_u32 s86, s46, s86
	s_addc_u32 s87, s47, 0
	v_mov_b32_e32 v254, 0
	global_load_dword v254, v254, s[86:87] sc1
	global_load_dwordx4 v[126:129], v[178:179], off
	global_load_dwordx4 v[174:177], v[178:179], off offset:1024
	global_load_dwordx4 v[192:195], v[178:179], off offset:2048
	global_load_dwordx4 v[196:199], v[178:179], off offset:3072
	v_lshl_add_u32 v163, s25, 10, v191
	ds_read_b128 v[200:203], v163
	ds_read_b128 v[204:207], v163 offset:16384
	ds_read_b128 v[208:211], v163 offset:32768
	ds_read_b128 v[212:215], v163 offset:49152
	s_setprio 1
	s_waitcnt vmcnt(12) lgkmcnt(3)
	v_mfma_f32_16x16x32_f16 v[66:69], v[18:21], v[200:203], v[66:69]
	s_waitcnt vmcnt(11)
	v_mfma_f32_16x16x32_f16 v[70:73], v[22:25], v[200:203], v[70:73]
	s_waitcnt vmcnt(10)
	v_mfma_f32_16x16x32_f16 v[74:77], v[26:29], v[200:203], v[74:77]
	s_waitcnt vmcnt(9)
	v_mfma_f32_16x16x32_f16 v[50:53], v[30:33], v[200:203], v[50:53]
	s_waitcnt lgkmcnt(2)
	v_mfma_f32_16x16x32_f16 v[78:81], v[18:21], v[204:207], v[78:81]
	v_mfma_f32_16x16x32_f16 v[82:85], v[22:25], v[204:207], v[82:85]
	v_mfma_f32_16x16x32_f16 v[86:89], v[26:29], v[204:207], v[86:89]
	v_mfma_f32_16x16x32_f16 v[54:57], v[30:33], v[204:207], v[54:57]
	s_waitcnt lgkmcnt(1)
	v_mfma_f32_16x16x32_f16 v[90:93], v[18:21], v[208:211], v[90:93]
	v_mfma_f32_16x16x32_f16 v[94:97], v[22:25], v[208:211], v[94:97]
	v_mfma_f32_16x16x32_f16 v[98:101], v[26:29], v[208:211], v[98:101]
	v_mfma_f32_16x16x32_f16 v[58:61], v[30:33], v[208:211], v[58:61]
	s_waitcnt lgkmcnt(0)
	v_mfma_f32_16x16x32_f16 v[102:105], v[18:21], v[212:215], v[102:105]
	v_mfma_f32_16x16x32_f16 v[106:109], v[22:25], v[212:215], v[106:109]
	v_mfma_f32_16x16x32_f16 v[110:113], v[26:29], v[212:215], v[110:113]
	v_mfma_f32_16x16x32_f16 v[62:65], v[30:33], v[212:215], v[62:65]
	s_setprio 0
	v_add_u32_e32 v165, 0x10000, v163
	v_add_u32_e32 v168, 0x14000, v163
	ds_read_b128 v[200:203], v165
	ds_read_b128 v[204:207], v168
	v_add_u32_e32 v165, 0x18000, v163
	v_add_u32_e32 v163, 0x1c000, v163
	ds_read_b128 v[208:211], v165
	ds_read_b128 v[212:215], v163
	s_setprio 1
	s_waitcnt lgkmcnt(3)
	v_mfma_f32_16x16x32_f16 v[130:133], v[18:21], v[200:203], v[130:133]
	v_mfma_f32_16x16x32_f16 v[134:137], v[22:25], v[200:203], v[134:137]
	v_mfma_f32_16x16x32_f16 v[138:141], v[26:29], v[200:203], v[138:141]
	v_mfma_f32_16x16x32_f16 v[114:117], v[30:33], v[200:203], v[114:117]
	s_waitcnt lgkmcnt(2)
	v_mfma_f32_16x16x32_f16 v[142:145], v[18:21], v[204:207], v[142:145]
	v_mfma_f32_16x16x32_f16 v[146:149], v[22:25], v[204:207], v[146:149]
	v_mfma_f32_16x16x32_f16 v[150:153], v[26:29], v[204:207], v[150:153]
	v_mfma_f32_16x16x32_f16 v[118:121], v[30:33], v[204:207], v[118:121]
	s_waitcnt lgkmcnt(1)
	v_mfma_f32_16x16x32_f16 v[154:157], v[18:21], v[208:211], v[154:157]
	v_mfma_f32_16x16x32_f16 v[158:161], v[22:25], v[208:211], v[158:161]
	v_mfma_f32_16x16x32_f16 v[122:125], v[30:33], v[208:211], v[122:125]
	s_waitcnt lgkmcnt(0)
	v_mfma_f32_16x16x32_f16 v[2:5], v[18:21], v[212:215], v[2:5]
	v_mfma_f32_16x16x32_f16 v[6:9], v[22:25], v[212:215], v[6:9]
	v_mfma_f32_16x16x32_f16 v[10:13], v[26:29], v[212:215], v[10:13]
	v_mfma_f32_16x16x32_f16 v[14:17], v[30:33], v[212:215], v[14:17]
	v_mfma_f32_16x16x32_f16 v[170:173], v[26:29], v[208:211], v[170:173]
	s_setprio 0
	s_add_i32 s0, s50, -1
	s_and_b32 s48, s0, 7
	s_or_b32 s25, s48, s2
	s_lshl_b32 s0, s25, 12
	v_lshl_add_u64 v[18:19], v[166:167], 0, s[0:1]
	global_load_dwordx4 v[200:203], v[18:19], off
	global_load_dwordx4 v[204:207], v[18:19], off offset:1024
	global_load_dwordx4 v[208:211], v[18:19], off offset:2048
	global_load_dwordx4 v[212:215], v[18:19], off offset:3072
	v_lshl_add_u32 v163, s49, 10, v191
	ds_read_b128 v[18:21], v163
	ds_read_b128 v[22:25], v163 offset:16384
	ds_read_b128 v[26:29], v163 offset:32768
	ds_read_b128 v[30:33], v163 offset:49152
	s_setprio 1
	s_waitcnt vmcnt(12) lgkmcnt(3)
	v_mfma_f32_16x16x32_f16 v[66:69], v[34:37], v[18:21], v[66:69]
	s_waitcnt vmcnt(11)
	v_mfma_f32_16x16x32_f16 v[70:73], v[38:41], v[18:21], v[70:73]
	s_waitcnt vmcnt(10)
	v_mfma_f32_16x16x32_f16 v[74:77], v[42:45], v[18:21], v[74:77]
	s_waitcnt vmcnt(9)
	v_mfma_f32_16x16x32_f16 v[18:21], v[46:49], v[18:21], v[50:53]
	s_waitcnt lgkmcnt(2)
	v_mfma_f32_16x16x32_f16 v[50:53], v[34:37], v[22:25], v[78:81]
	v_mfma_f32_16x16x32_f16 v[78:81], v[38:41], v[22:25], v[82:85]
	v_mfma_f32_16x16x32_f16 v[82:85], v[42:45], v[22:25], v[86:89]
	v_mfma_f32_16x16x32_f16 v[22:25], v[46:49], v[22:25], v[54:57]
	s_waitcnt lgkmcnt(1)
	v_mfma_f32_16x16x32_f16 v[54:57], v[34:37], v[26:29], v[90:93]
	v_mfma_f32_16x16x32_f16 v[86:89], v[38:41], v[26:29], v[94:97]
	v_mfma_f32_16x16x32_f16 v[90:93], v[42:45], v[26:29], v[98:101]
	v_mfma_f32_16x16x32_f16 v[26:29], v[46:49], v[26:29], v[58:61]
	s_waitcnt lgkmcnt(0)
	v_mfma_f32_16x16x32_f16 v[58:61], v[34:37], v[30:33], v[102:105]
	v_mfma_f32_16x16x32_f16 v[94:97], v[38:41], v[30:33], v[106:109]
	v_mfma_f32_16x16x32_f16 v[98:101], v[42:45], v[30:33], v[110:113]
	v_mfma_f32_16x16x32_f16 v[30:33], v[46:49], v[30:33], v[62:65]
	s_setprio 0
	s_nop 1
	v_add_u32_e32 v62, 0x10000, v163
	v_add_u32_e32 v102, 0x14000, v163
	v_add_u32_e32 v106, 0x18000, v163
	v_add_u32_e32 v110, 0x1c000, v163
	ds_read_b128 v[62:65], v62
	ds_read_b128 v[102:105], v102
	ds_read_b128 v[106:109], v106
	ds_read_b128 v[110:113], v110
	s_setprio 1
	s_waitcnt lgkmcnt(3)
	v_mfma_f32_16x16x32_f16 v[130:133], v[34:37], v[62:65], v[130:133]
	v_mfma_f32_16x16x32_f16 v[134:137], v[38:41], v[62:65], v[134:137]
	v_mfma_f32_16x16x32_f16 v[138:141], v[42:45], v[62:65], v[138:141]
	v_mfma_f32_16x16x32_f16 v[62:65], v[46:49], v[62:65], v[114:117]
	s_waitcnt lgkmcnt(2)
	v_mfma_f32_16x16x32_f16 v[114:117], v[34:37], v[102:105], v[142:145]
	v_mfma_f32_16x16x32_f16 v[142:145], v[38:41], v[102:105], v[146:149]
	v_mfma_f32_16x16x32_f16 v[146:149], v[42:45], v[102:105], v[150:153]
	v_mfma_f32_16x16x32_f16 v[102:105], v[46:49], v[102:105], v[118:121]
	s_waitcnt lgkmcnt(1)
	v_mfma_f32_16x16x32_f16 v[118:121], v[34:37], v[106:109], v[154:157]
	v_mfma_f32_16x16x32_f16 v[150:153], v[38:41], v[106:109], v[158:161]
	v_mfma_f32_16x16x32_f16 v[154:157], v[42:45], v[106:109], v[170:173]
	v_mfma_f32_16x16x32_f16 v[106:109], v[46:49], v[106:109], v[122:125]
	s_waitcnt lgkmcnt(0)
	v_mfma_f32_16x16x32_f16 v[34:37], v[34:37], v[110:113], v[2:5]
	v_mfma_f32_16x16x32_f16 v[38:41], v[38:41], v[110:113], v[6:9]
	v_mfma_f32_16x16x32_f16 v[42:45], v[42:45], v[110:113], v[10:13]
	v_mfma_f32_16x16x32_f16 v[46:49], v[46:49], v[110:113], v[14:17]
	s_setprio 0
	s_xor_b32 s2, s58, 1
	s_lshl_b32 s49, s2, 3
	s_or_b32 s51, s49, s50
	s_lshl_b32 s0, s51, 12
	v_lshl_add_u64 v[14:15], v[166:167], 0, s[0:1]
	s_waitcnt vmcnt(8)
	s_barrier
	v_lshlrev_b32_e32 v255, 4, v0
	v_readfirstlane_b32 s92, v0
	s_lshl_b32 s92, s92, 4
	s_xor_b32 s93, s58, 1
	s_lshl_b32 s94, s93, 13
	s_add_i32 s92, s92, s94
	s_lshl_b32 s94, s34, 3
	s_or_b32 s94, s94, s33
	s_xor_b32 s94, s94, 1
	s_lshl_b32 s94, s94, 16
	s_add_u32 s88, s26, s94
	s_addc_u32 s89, s27, 0
	s_add_i32 s95, s92, 0x0
	s_mov_b32 m0, s95
	s_add_u32 s84, s88, 0x0
	s_addc_u32 s85, s89, 0
	global_load_lds_dwordx4 v255, s[84:85] sc0 sc1
	s_add_i32 s95, s92, 0x4000
	s_mov_b32 m0, s95
	s_add_u32 s84, s88, 0x2000
	s_addc_u32 s85, s89, 0
	global_load_lds_dwordx4 v255, s[84:85] sc0 sc1
	s_add_i32 s95, s92, 0x8000
	s_mov_b32 m0, s95
	s_add_u32 s84, s88, 0x4000
	s_addc_u32 s85, s89, 0
	global_load_lds_dwordx4 v255, s[84:85] sc0 sc1
	s_add_i32 s95, s92, 0xc000
	s_mov_b32 m0, s95
	s_add_u32 s84, s88, 0x6000
	s_addc_u32 s85, s89, 0
	global_load_lds_dwordx4 v255, s[84:85] sc0 sc1
	s_add_i32 s95, s92, 0x10000
	s_mov_b32 m0, s95
	s_add_u32 s84, s88, 0x8000
	s_addc_u32 s85, s89, 0
	global_load_lds_dwordx4 v255, s[84:85] sc0 sc1
	s_add_i32 s95, s92, 0x14000
	s_mov_b32 m0, s95
	s_add_u32 s84, s88, 0xa000
	s_addc_u32 s85, s89, 0
	global_load_lds_dwordx4 v255, s[84:85] sc0 sc1
	s_add_i32 s95, s92, 0x18000
	s_mov_b32 m0, s95
	s_add_u32 s84, s88, 0xc000
	s_addc_u32 s85, s89, 0
	global_load_lds_dwordx4 v255, s[84:85] sc0 sc1
	s_add_i32 s95, s92, 0x1c000
	s_mov_b32 m0, s95
	s_add_u32 s84, s88, 0xe000
	s_addc_u32 s85, s89, 0
	global_load_lds_dwordx4 v255, s[84:85] sc0 sc1
	s_cmp_eq_u32 s98, 0
	s_cbranch_scc1 .Lstag_3
	s_sleep 4
.Lstag_3:
	global_load_dwordx4 v[2:5], v[14:15], off
	global_load_dwordx4 v[6:9], v[14:15], off offset:1024
	global_load_dwordx4 v[10:13], v[14:15], off offset:2048
	s_nop 0
	global_load_dwordx4 v[14:17], v[14:15], off offset:3072
	v_lshl_add_u32 v163, s52, 10, v191
	ds_read_b128 v[110:113], v163
	ds_read_b128 v[122:125], v163 offset:16384
	ds_read_b128 v[158:161], v163 offset:32768
	ds_read_b128 v[170:173], v163 offset:49152
	s_setprio 1
	s_waitcnt vmcnt(19) lgkmcnt(3)
	v_mfma_f32_16x16x32_f16 v[66:69], v[126:129], v[110:113], v[66:69]
	s_waitcnt vmcnt(18)
	v_mfma_f32_16x16x32_f16 v[70:73], v[174:177], v[110:113], v[70:73]
	s_waitcnt vmcnt(17)
	v_mfma_f32_16x16x32_f16 v[74:77], v[192:195], v[110:113], v[74:77]
	s_waitcnt vmcnt(16)
	v_mfma_f32_16x16x32_f16 v[110:113], v[196:199], v[110:113], v[18:21]
	s_waitcnt lgkmcnt(2)
	v_mfma_f32_16x16x32_f16 v[50:53], v[126:129], v[122:125], v[50:53]
	v_mfma_f32_16x16x32_f16 v[78:81], v[174:177], v[122:125], v[78:81]
	v_mfma_f32_16x16x32_f16 v[82:85], v[192:195], v[122:125], v[82:85]
	v_mfma_f32_16x16x32_f16 v[122:125], v[196:199], v[122:125], v[22:25]
	s_waitcnt lgkmcnt(1)
	v_mfma_f32_16x16x32_f16 v[216:219], v[126:129], v[158:161], v[54:57]
	v_mfma_f32_16x16x32_f16 v[86:89], v[174:177], v[158:161], v[86:89]
	v_mfma_f32_16x16x32_f16 v[90:93], v[192:195], v[158:161], v[90:93]
	v_mfma_f32_16x16x32_f16 v[158:161], v[196:199], v[158:161], v[26:29]
	s_waitcnt lgkmcnt(0)
	v_mfma_f32_16x16x32_f16 v[94:97], v[174:177], v[170:173], v[94:97]
	v_mfma_f32_16x16x32_f16 v[98:101], v[192:195], v[170:173], v[98:101]
	v_mfma_f32_16x16x32_f16 v[220:223], v[126:129], v[170:173], v[58:61]
	v_mfma_f32_16x16x32_f16 v[170:173], v[196:199], v[170:173], v[30:33]
	s_setprio 0
	v_add_u32_e32 v18, 0x10000, v163
	v_add_u32_e32 v22, 0x14000, v163
	v_add_u32_e32 v26, 0x18000, v163
	v_add_u32_e32 v30, 0x1c000, v163
	ds_read_b128 v[18:21], v18
	ds_read_b128 v[22:25], v22
	ds_read_b128 v[26:29], v26
	ds_read_b128 v[30:33], v30
	s_setprio 1
	s_waitcnt lgkmcnt(3)
	v_mfma_f32_16x16x32_f16 v[130:133], v[126:129], v[18:21], v[130:133]
	v_mfma_f32_16x16x32_f16 v[134:137], v[174:177], v[18:21], v[134:137]
	v_mfma_f32_16x16x32_f16 v[138:141], v[192:195], v[18:21], v[138:141]
	s_waitcnt lgkmcnt(2)
	v_mfma_f32_16x16x32_f16 v[114:117], v[126:129], v[22:25], v[114:117]
	v_mfma_f32_16x16x32_f16 v[142:145], v[174:177], v[22:25], v[142:145]
	v_mfma_f32_16x16x32_f16 v[146:149], v[192:195], v[22:25], v[146:149]
	s_waitcnt lgkmcnt(1)
	v_mfma_f32_16x16x32_f16 v[150:153], v[174:177], v[26:29], v[150:153]
	v_mfma_f32_16x16x32_f16 v[154:157], v[192:195], v[26:29], v[154:157]
	v_mfma_f32_16x16x32_f16 v[224:227], v[196:199], v[18:21], v[62:65]
	v_mfma_f32_16x16x32_f16 v[228:231], v[196:199], v[22:25], v[102:105]
	v_mfma_f32_16x16x32_f16 v[232:235], v[126:129], v[26:29], v[118:121]
	v_mfma_f32_16x16x32_f16 v[236:239], v[196:199], v[26:29], v[106:109]
	s_waitcnt lgkmcnt(0)
	v_mfma_f32_16x16x32_f16 v[240:243], v[126:129], v[30:33], v[34:37]
	v_mfma_f32_16x16x32_f16 v[174:177], v[174:177], v[30:33], v[38:41]
	v_mfma_f32_16x16x32_f16 v[192:195], v[192:195], v[30:33], v[42:45]
	v_mfma_f32_16x16x32_f16 v[196:199], v[196:199], v[30:33], v[46:49]
	s_setprio 0
	s_or_b32 s52, s49, s24
	s_lshl_b32 s0, s52, 12
	v_lshl_add_u64 v[30:31], v[166:167], 0, s[0:1]
	global_load_dwordx4 v[18:21], v[30:31], off
	global_load_dwordx4 v[22:25], v[30:31], off offset:1024
	global_load_dwordx4 v[26:29], v[30:31], off offset:2048
	s_nop 0
	global_load_dwordx4 v[30:33], v[30:31], off offset:3072
	v_lshl_add_u32 v118, s25, 10, v191
	ds_read_b128 v[46:49], v118
	ds_read_b128 v[62:65], v118 offset:16384
	ds_read_b128 v[102:105], v118 offset:32768
	ds_read_b128 v[106:109], v118 offset:49152
	s_setprio 1
	s_waitcnt vmcnt(19) lgkmcnt(3)
	v_mfma_f32_16x16x32_f16 v[34:37], v[200:203], v[46:49], v[66:69]
	s_waitcnt vmcnt(18)
	v_mfma_f32_16x16x32_f16 v[38:41], v[204:207], v[46:49], v[70:73]
	s_waitcnt vmcnt(17)
	v_mfma_f32_16x16x32_f16 v[42:45], v[208:211], v[46:49], v[74:77]
	s_waitcnt vmcnt(16)
	v_mfma_f32_16x16x32_f16 v[46:49], v[212:215], v[46:49], v[110:113]
	s_waitcnt lgkmcnt(2)
	v_mfma_f32_16x16x32_f16 v[50:53], v[200:203], v[62:65], v[50:53]
	v_mfma_f32_16x16x32_f16 v[54:57], v[204:207], v[62:65], v[78:81]
	v_mfma_f32_16x16x32_f16 v[58:61], v[208:211], v[62:65], v[82:85]
	v_mfma_f32_16x16x32_f16 v[62:65], v[212:215], v[62:65], v[122:125]
	s_waitcnt lgkmcnt(1)
	v_mfma_f32_16x16x32_f16 v[66:69], v[200:203], v[102:105], v[216:219]
	v_mfma_f32_16x16x32_f16 v[70:73], v[204:207], v[102:105], v[86:89]
	v_mfma_f32_16x16x32_f16 v[74:77], v[208:211], v[102:105], v[90:93]
	v_mfma_f32_16x16x32_f16 v[78:81], v[212:215], v[102:105], v[158:161]
	s_waitcnt lgkmcnt(0)
	v_mfma_f32_16x16x32_f16 v[82:85], v[200:203], v[106:109], v[220:223]
	v_mfma_f32_16x16x32_f16 v[86:89], v[204:207], v[106:109], v[94:97]
	v_mfma_f32_16x16x32_f16 v[90:93], v[208:211], v[106:109], v[98:101]
	v_mfma_f32_16x16x32_f16 v[94:97], v[212:215], v[106:109], v[170:173]
	s_setprio 0
	s_nop 0
	v_add_u32_e32 v98, 0x10000, v118
	v_add_u32_e32 v99, 0x14000, v118
	ds_read_b128 v[110:113], v98
	ds_read_b128 v[126:129], v99
	v_add_u32_e32 v98, 0x18000, v118
	v_add_u32_e32 v99, 0x1c000, v118
	ds_read_b128 v[158:161], v98
	ds_read_b128 v[170:173], v99
	s_setprio 1
	s_waitcnt lgkmcnt(3)
	v_mfma_f32_16x16x32_f16 v[98:101], v[200:203], v[110:113], v[130:133]
	v_mfma_f32_16x16x32_f16 v[102:105], v[204:207], v[110:113], v[134:137]
	v_mfma_f32_16x16x32_f16 v[106:109], v[208:211], v[110:113], v[138:141]
	v_mfma_f32_16x16x32_f16 v[110:113], v[212:215], v[110:113], v[224:227]
	s_waitcnt lgkmcnt(2)
	v_mfma_f32_16x16x32_f16 v[114:117], v[200:203], v[126:129], v[114:117]
	v_mfma_f32_16x16x32_f16 v[118:121], v[204:207], v[126:129], v[142:145]
	v_mfma_f32_16x16x32_f16 v[122:125], v[208:211], v[126:129], v[146:149]
	v_mfma_f32_16x16x32_f16 v[126:129], v[212:215], v[126:129], v[228:231]
	s_waitcnt lgkmcnt(1)
	v_mfma_f32_16x16x32_f16 v[130:133], v[200:203], v[158:161], v[232:235]
	v_mfma_f32_16x16x32_f16 v[134:137], v[204:207], v[158:161], v[150:153]
	v_mfma_f32_16x16x32_f16 v[138:141], v[208:211], v[158:161], v[154:157]
	v_mfma_f32_16x16x32_f16 v[142:145], v[212:215], v[158:161], v[236:239]
	s_waitcnt lgkmcnt(0)
	v_mfma_f32_16x16x32_f16 v[146:149], v[200:203], v[170:173], v[240:243]
	v_mfma_f32_16x16x32_f16 v[150:153], v[204:207], v[170:173], v[174:177]
	v_mfma_f32_16x16x32_f16 v[154:157], v[208:211], v[170:173], v[192:195]
	v_mfma_f32_16x16x32_f16 v[158:161], v[212:215], v[170:173], v[196:199]
	s_setprio 0
	s_waitcnt vmcnt(0)
	s_barrier
	s_getreg_b32 s24, hwreg(HW_REG_XCC_ID, 0, 4)
	s_and_saveexec_b64 s[0:1], s[4:5]
	s_cbranch_execz .LBB5_145
	s_and_b32 s53, s24, 15
	s_lshl_b32 s24, s34, 3
	s_or_b32 s50, s24, s50
	s_or_b32 s24, s50, s58
	s_lshl_b32 s24, s24, 5
	s_ashr_i32 s25, s24, 31
	s_lshl_b64 s[24:25], s[24:25], 2
	s_add_u32 s24, s46, s24
	s_addc_u32 s25, s47, s25
	s_add_i32 s54, s53, 1
	v_mov_b32_e32 v163, s54
	s_or_b32 s24, s50, s2
	s_lshl_b32 s24, s24, 5
	s_ashr_i32 s25, s24, 31
	s_lshl_b64 s[24:25], s[24:25], 2
	s_add_u32 s24, s46, s24
	s_addc_u32 s25, s47, s25
	s_mov_b32 s90, 0
	v_mov_b32_e32 v163, v254
	v_cmp_ne_u32_e32 vcc, 0, v163
	s_cbranch_vccnz .LBB5_144
	s_mov_b32 s90, 2
	v_mov_b32_e32 v165, 0

.Lex_skip:
.LBB5_148:
	s_or_b32 s2, s49, s28
	s_lshl_b32 s0, s2, 12
	s_mov_b32 s1, 0
	v_lshl_add_u64 v[176:177], v[166:167], 0, s[0:1]
	s_waitcnt vmcnt(0)
	s_waitcnt vmcnt(0) lgkmcnt(0)
	s_barrier
	global_load_dwordx4 v[162:165], v[176:177], off
	global_load_dwordx4 v[168:171], v[176:177], off offset:1024
	global_load_dwordx4 v[172:175], v[176:177], off offset:2048
	s_nop 0
	global_load_dwordx4 v[176:179], v[176:177], off offset:3072
	s_cmp_eq_u32 s98, 0
	s_cbranch_scc1 .Lstag_4
	s_sleep 4
.Lstag_4:
	v_lshl_add_u32 v208, s51, 10, v191
	ds_read_b128 v[192:195], v208
	ds_read_b128 v[196:199], v208 offset:16384
	ds_read_b128 v[200:203], v208 offset:32768
	ds_read_b128 v[204:207], v208 offset:49152
	s_setprio 1
	s_waitcnt lgkmcnt(3)
	v_mfma_f32_16x16x32_f16 v[34:37], v[2:5], v[192:195], v[34:37]
	v_mfma_f32_16x16x32_f16 v[38:41], v[6:9], v[192:195], v[38:41]
	v_mfma_f32_16x16x32_f16 v[42:45], v[10:13], v[192:195], v[42:45]
	v_mfma_f32_16x16x32_f16 v[46:49], v[14:17], v[192:195], v[46:49]
	s_waitcnt lgkmcnt(2)
	v_mfma_f32_16x16x32_f16 v[50:53], v[2:5], v[196:199], v[50:53]
	v_mfma_f32_16x16x32_f16 v[54:57], v[6:9], v[196:199], v[54:57]
	v_mfma_f32_16x16x32_f16 v[58:61], v[10:13], v[196:199], v[58:61]
	v_mfma_f32_16x16x32_f16 v[62:65], v[14:17], v[196:199], v[62:65]
	s_waitcnt lgkmcnt(1)
	v_mfma_f32_16x16x32_f16 v[66:69], v[2:5], v[200:203], v[66:69]
	v_mfma_f32_16x16x32_f16 v[70:73], v[6:9], v[200:203], v[70:73]
	v_mfma_f32_16x16x32_f16 v[74:77], v[10:13], v[200:203], v[74:77]
	v_mfma_f32_16x16x32_f16 v[78:81], v[14:17], v[200:203], v[78:81]
	s_waitcnt lgkmcnt(0)
	v_mfma_f32_16x16x32_f16 v[82:85], v[2:5], v[204:207], v[82:85]
	v_mfma_f32_16x16x32_f16 v[86:89], v[6:9], v[204:207], v[86:89]
	v_mfma_f32_16x16x32_f16 v[90:93], v[10:13], v[204:207], v[90:93]
	v_mfma_f32_16x16x32_f16 v[94:97], v[14:17], v[204:207], v[94:97]
	s_setprio 0
	v_add_u32_e32 v192, 0x10000, v208
	v_add_u32_e32 v196, 0x14000, v208
	v_add_u32_e32 v200, 0x18000, v208
	v_add_u32_e32 v204, 0x1c000, v208
	ds_read_b128 v[192:195], v192
	ds_read_b128 v[196:199], v196
	ds_read_b128 v[200:203], v200
	ds_read_b128 v[204:207], v204
	s_setprio 1
	s_waitcnt lgkmcnt(3)
	v_mfma_f32_16x16x32_f16 v[98:101], v[2:5], v[192:195], v[98:101]
	v_mfma_f32_16x16x32_f16 v[102:105], v[6:9], v[192:195], v[102:105]
	v_mfma_f32_16x16x32_f16 v[106:109], v[10:13], v[192:195], v[106:109]
	v_mfma_f32_16x16x32_f16 v[110:113], v[14:17], v[192:195], v[110:113]
	s_waitcnt lgkmcnt(2)
	v_mfma_f32_16x16x32_f16 v[114:117], v[2:5], v[196:199], v[114:117]
	v_mfma_f32_16x16x32_f16 v[118:121], v[6:9], v[196:199], v[118:121]
	v_mfma_f32_16x16x32_f16 v[122:125], v[10:13], v[196:199], v[122:125]
	v_mfma_f32_16x16x32_f16 v[126:129], v[14:17], v[196:199], v[126:129]
	s_waitcnt lgkmcnt(1)
	v_mfma_f32_16x16x32_f16 v[130:133], v[2:5], v[200:203], v[130:133]
	v_mfma_f32_16x16x32_f16 v[134:137], v[6:9], v[200:203], v[134:137]
	v_mfma_f32_16x16x32_f16 v[138:141], v[10:13], v[200:203], v[138:141]
	v_mfma_f32_16x16x32_f16 v[142:145], v[14:17], v[200:203], v[142:145]
	s_waitcnt lgkmcnt(0)
	v_mfma_f32_16x16x32_f16 v[2:5], v[2:5], v[204:207], v[146:149]
	v_mfma_f32_16x16x32_f16 v[6:9], v[6:9], v[204:207], v[150:153]
	v_mfma_f32_16x16x32_f16 v[10:13], v[10:13], v[204:207], v[154:157]
	v_mfma_f32_16x16x32_f16 v[14:17], v[14:17], v[204:207], v[158:161]
	s_setprio 0
	s_or_b32 s3, s49, s29
	s_lshl_b32 s0, s3, 12
	v_lshl_add_u64 v[158:159], v[166:167], 0, s[0:1]
	global_load_dwordx4 v[146:149], v[158:159], off
	global_load_dwordx4 v[150:153], v[158:159], off offset:1024
	global_load_dwordx4 v[154:157], v[158:159], off offset:2048
	s_nop 0
	global_load_dwordx4 v[158:161], v[158:159], off offset:3072
	v_lshl_add_u32 v208, s52, 10, v191
	ds_read_b128 v[192:195], v208
	ds_read_b128 v[196:199], v208 offset:16384
	ds_read_b128 v[200:203], v208 offset:32768
	ds_read_b128 v[204:207], v208 offset:49152
	s_setprio 1
	s_waitcnt lgkmcnt(3)
	v_mfma_f32_16x16x32_f16 v[34:37], v[18:21], v[192:195], v[34:37]
	v_mfma_f32_16x16x32_f16 v[38:41], v[22:25], v[192:195], v[38:41]
	v_mfma_f32_16x16x32_f16 v[42:45], v[26:29], v[192:195], v[42:45]
	v_mfma_f32_16x16x32_f16 v[46:49], v[30:33], v[192:195], v[46:49]
	s_waitcnt lgkmcnt(2)
	v_mfma_f32_16x16x32_f16 v[50:53], v[18:21], v[196:199], v[50:53]
	v_mfma_f32_16x16x32_f16 v[54:57], v[22:25], v[196:199], v[54:57]
	v_mfma_f32_16x16x32_f16 v[58:61], v[26:29], v[196:199], v[58:61]
	v_mfma_f32_16x16x32_f16 v[62:65], v[30:33], v[196:199], v[62:65]
	s_waitcnt lgkmcnt(1)
	v_mfma_f32_16x16x32_f16 v[66:69], v[18:21], v[200:203], v[66:69]
	v_mfma_f32_16x16x32_f16 v[70:73], v[22:25], v[200:203], v[70:73]
	v_mfma_f32_16x16x32_f16 v[74:77], v[26:29], v[200:203], v[74:77]
	v_mfma_f32_16x16x32_f16 v[78:81], v[30:33], v[200:203], v[78:81]
	s_waitcnt lgkmcnt(0)
	v_mfma_f32_16x16x32_f16 v[82:85], v[18:21], v[204:207], v[82:85]
	v_mfma_f32_16x16x32_f16 v[86:89], v[22:25], v[204:207], v[86:89]
	v_mfma_f32_16x16x32_f16 v[90:93], v[26:29], v[204:207], v[90:93]
	v_mfma_f32_16x16x32_f16 v[94:97], v[30:33], v[204:207], v[94:97]
	s_setprio 0
	v_add_u32_e32 v192, 0x10000, v208
	v_add_u32_e32 v196, 0x14000, v208
	v_add_u32_e32 v200, 0x18000, v208
	v_add_u32_e32 v204, 0x1c000, v208
	ds_read_b128 v[192:195], v192
	ds_read_b128 v[196:199], v196
	ds_read_b128 v[200:203], v200
	ds_read_b128 v[204:207], v204
	s_setprio 1
	s_waitcnt lgkmcnt(3)
	v_mfma_f32_16x16x32_f16 v[98:101], v[18:21], v[192:195], v[98:101]
	v_mfma_f32_16x16x32_f16 v[102:105], v[22:25], v[192:195], v[102:105]
	v_mfma_f32_16x16x32_f16 v[106:109], v[26:29], v[192:195], v[106:109]
	v_mfma_f32_16x16x32_f16 v[110:113], v[30:33], v[192:195], v[110:113]
	s_waitcnt lgkmcnt(2)
	v_mfma_f32_16x16x32_f16 v[114:117], v[18:21], v[196:199], v[114:117]
	v_mfma_f32_16x16x32_f16 v[118:121], v[22:25], v[196:199], v[118:121]
	v_mfma_f32_16x16x32_f16 v[122:125], v[26:29], v[196:199], v[122:125]
	v_mfma_f32_16x16x32_f16 v[126:129], v[30:33], v[196:199], v[126:129]
	s_waitcnt lgkmcnt(1)
	v_mfma_f32_16x16x32_f16 v[130:133], v[18:21], v[200:203], v[130:133]
	v_mfma_f32_16x16x32_f16 v[134:137], v[22:25], v[200:203], v[134:137]
	v_mfma_f32_16x16x32_f16 v[138:141], v[26:29], v[200:203], v[138:141]
	s_waitcnt lgkmcnt(0)
	v_mfma_f32_16x16x32_f16 v[2:5], v[18:21], v[204:207], v[2:5]
	v_mfma_f32_16x16x32_f16 v[6:9], v[22:25], v[204:207], v[6:9]
	v_mfma_f32_16x16x32_f16 v[10:13], v[26:29], v[204:207], v[10:13]
	v_mfma_f32_16x16x32_f16 v[14:17], v[30:33], v[204:207], v[14:17]
	v_mfma_f32_16x16x32_f16 v[142:145], v[30:33], v[200:203], v[142:145]
	s_setprio 0
	s_xor_b32 s7, s51, 4
	s_lshl_b32 s0, s7, 12
	v_lshl_add_u64 v[30:31], v[166:167], 0, s[0:1]
	global_load_dwordx4 v[18:21], v[30:31], off
	global_load_dwordx4 v[22:25], v[30:31], off offset:1024
	global_load_dwordx4 v[26:29], v[30:31], off offset:2048
	s_nop 0
	global_load_dwordx4 v[30:33], v[30:31], off offset:3072
	v_lshl_add_u32 v208, s2, 10, v191
	ds_read_b128 v[192:195], v208
	ds_read_b128 v[196:199], v208 offset:16384
	ds_read_b128 v[200:203], v208 offset:32768
	ds_read_b128 v[204:207], v208 offset:49152
	s_setprio 1
	s_waitcnt vmcnt(11) lgkmcnt(3)
	v_mfma_f32_16x16x32_f16 v[34:37], v[162:165], v[192:195], v[34:37]
	s_waitcnt vmcnt(10)
	v_mfma_f32_16x16x32_f16 v[38:41], v[168:171], v[192:195], v[38:41]
	s_waitcnt vmcnt(9)
	v_mfma_f32_16x16x32_f16 v[42:45], v[172:175], v[192:195], v[42:45]
	s_waitcnt vmcnt(8)
	v_mfma_f32_16x16x32_f16 v[46:49], v[176:179], v[192:195], v[46:49]
	s_waitcnt lgkmcnt(2)
	v_mfma_f32_16x16x32_f16 v[50:53], v[162:165], v[196:199], v[50:53]
	v_mfma_f32_16x16x32_f16 v[54:57], v[168:171], v[196:199], v[54:57]
	v_mfma_f32_16x16x32_f16 v[58:61], v[172:175], v[196:199], v[58:61]
	v_mfma_f32_16x16x32_f16 v[62:65], v[176:179], v[196:199], v[62:65]
	s_waitcnt lgkmcnt(1)
	v_mfma_f32_16x16x32_f16 v[66:69], v[162:165], v[200:203], v[66:69]
	v_mfma_f32_16x16x32_f16 v[70:73], v[168:171], v[200:203], v[70:73]
	v_mfma_f32_16x16x32_f16 v[74:77], v[172:175], v[200:203], v[74:77]
	v_mfma_f32_16x16x32_f16 v[78:81], v[176:179], v[200:203], v[78:81]
	s_waitcnt lgkmcnt(0)
	v_mfma_f32_16x16x32_f16 v[82:85], v[162:165], v[204:207], v[82:85]
	v_mfma_f32_16x16x32_f16 v[86:89], v[168:171], v[204:207], v[86:89]
	v_mfma_f32_16x16x32_f16 v[90:93], v[172:175], v[204:207], v[90:93]
	v_mfma_f32_16x16x32_f16 v[94:97], v[176:179], v[204:207], v[94:97]
	s_setprio 0
	v_add_u32_e32 v192, 0x10000, v208
	v_add_u32_e32 v196, 0x14000, v208
	v_add_u32_e32 v200, 0x18000, v208
	v_add_u32_e32 v204, 0x1c000, v208
	ds_read_b128 v[192:195], v192
	ds_read_b128 v[196:199], v196
	ds_read_b128 v[200:203], v200
	ds_read_b128 v[204:207], v204
	s_setprio 1
	s_waitcnt lgkmcnt(3)
	v_mfma_f32_16x16x32_f16 v[98:101], v[162:165], v[192:195], v[98:101]
	v_mfma_f32_16x16x32_f16 v[102:105], v[168:171], v[192:195], v[102:105]
	v_mfma_f32_16x16x32_f16 v[106:109], v[172:175], v[192:195], v[106:109]
	v_mfma_f32_16x16x32_f16 v[110:113], v[176:179], v[192:195], v[110:113]
	s_waitcnt lgkmcnt(2)
	v_mfma_f32_16x16x32_f16 v[114:117], v[162:165], v[196:199], v[114:117]
	v_mfma_f32_16x16x32_f16 v[118:121], v[168:171], v[196:199], v[118:121]
	v_mfma_f32_16x16x32_f16 v[122:125], v[172:175], v[196:199], v[122:125]
	v_mfma_f32_16x16x32_f16 v[126:129], v[176:179], v[196:199], v[126:129]
	s_waitcnt lgkmcnt(1)
	v_mfma_f32_16x16x32_f16 v[130:133], v[162:165], v[200:203], v[130:133]
	v_mfma_f32_16x16x32_f16 v[134:137], v[168:171], v[200:203], v[134:137]
	v_mfma_f32_16x16x32_f16 v[138:141], v[172:175], v[200:203], v[138:141]
	s_waitcnt lgkmcnt(0)
	v_mfma_f32_16x16x32_f16 v[2:5], v[162:165], v[204:207], v[2:5]
	v_mfma_f32_16x16x32_f16 v[6:9], v[168:171], v[204:207], v[6:9]
	v_mfma_f32_16x16x32_f16 v[10:13], v[172:175], v[204:207], v[10:13]
	v_mfma_f32_16x16x32_f16 v[14:17], v[176:179], v[204:207], v[14:17]
	v_mfma_f32_16x16x32_f16 v[142:145], v[176:179], v[200:203], v[142:145]
	s_setprio 0
	s_or_b32 s2, s49, s30
	s_lshl_b32 s0, s2, 12
	v_lshl_add_u64 v[176:177], v[166:167], 0, s[0:1]
	global_load_dwordx4 v[162:165], v[176:177], off
	global_load_dwordx4 v[168:171], v[176:177], off offset:1024
	global_load_dwordx4 v[172:175], v[176:177], off offset:2048
	s_nop 0
	global_load_dwordx4 v[176:179], v[176:177], off offset:3072
	v_lshl_add_u32 v208, s3, 10, v191
	ds_read_b128 v[192:195], v208
	ds_read_b128 v[196:199], v208 offset:16384
	ds_read_b128 v[200:203], v208 offset:32768
	ds_read_b128 v[204:207], v208 offset:49152
	s_setprio 1
	s_waitcnt vmcnt(11) lgkmcnt(3)
	v_mfma_f32_16x16x32_f16 v[34:37], v[146:149], v[192:195], v[34:37]
	s_waitcnt vmcnt(10)
	v_mfma_f32_16x16x32_f16 v[38:41], v[150:153], v[192:195], v[38:41]
	s_waitcnt vmcnt(9)
	v_mfma_f32_16x16x32_f16 v[42:45], v[154:157], v[192:195], v[42:45]
	s_waitcnt vmcnt(8)
	v_mfma_f32_16x16x32_f16 v[46:49], v[158:161], v[192:195], v[46:49]
	s_waitcnt lgkmcnt(2)
	v_mfma_f32_16x16x32_f16 v[50:53], v[146:149], v[196:199], v[50:53]
	v_mfma_f32_16x16x32_f16 v[54:57], v[150:153], v[196:199], v[54:57]
	v_mfma_f32_16x16x32_f16 v[58:61], v[154:157], v[196:199], v[58:61]
	v_mfma_f32_16x16x32_f16 v[62:65], v[158:161], v[196:199], v[62:65]
	s_waitcnt lgkmcnt(1)
	v_mfma_f32_16x16x32_f16 v[66:69], v[146:149], v[200:203], v[66:69]
	v_mfma_f32_16x16x32_f16 v[70:73], v[150:153], v[200:203], v[70:73]
	v_mfma_f32_16x16x32_f16 v[74:77], v[154:157], v[200:203], v[74:77]
	v_mfma_f32_16x16x32_f16 v[78:81], v[158:161], v[200:203], v[78:81]
	s_waitcnt lgkmcnt(0)
	v_mfma_f32_16x16x32_f16 v[82:85], v[146:149], v[204:207], v[82:85]
	v_mfma_f32_16x16x32_f16 v[86:89], v[150:153], v[204:207], v[86:89]
	v_mfma_f32_16x16x32_f16 v[90:93], v[154:157], v[204:207], v[90:93]
	v_mfma_f32_16x16x32_f16 v[94:97], v[158:161], v[204:207], v[94:97]
	s_setprio 0
	v_add_u32_e32 v192, 0x10000, v208
	v_add_u32_e32 v196, 0x14000, v208
	v_add_u32_e32 v200, 0x18000, v208
	v_add_u32_e32 v204, 0x1c000, v208
	ds_read_b128 v[192:195], v192
	ds_read_b128 v[196:199], v196
	ds_read_b128 v[200:203], v200
	ds_read_b128 v[204:207], v204
	s_setprio 1
	s_waitcnt lgkmcnt(3)
	v_mfma_f32_16x16x32_f16 v[98:101], v[146:149], v[192:195], v[98:101]
	v_mfma_f32_16x16x32_f16 v[102:105], v[150:153], v[192:195], v[102:105]
	v_mfma_f32_16x16x32_f16 v[106:109], v[154:157], v[192:195], v[106:109]
	v_mfma_f32_16x16x32_f16 v[110:113], v[158:161], v[192:195], v[110:113]
	s_waitcnt lgkmcnt(2)
	v_mfma_f32_16x16x32_f16 v[114:117], v[146:149], v[196:199], v[114:117]
	v_mfma_f32_16x16x32_f16 v[118:121], v[150:153], v[196:199], v[118:121]
	v_mfma_f32_16x16x32_f16 v[122:125], v[154:157], v[196:199], v[122:125]
	v_mfma_f32_16x16x32_f16 v[126:129], v[158:161], v[196:199], v[126:129]
	s_waitcnt lgkmcnt(1)
	v_mfma_f32_16x16x32_f16 v[130:133], v[146:149], v[200:203], v[130:133]
	v_mfma_f32_16x16x32_f16 v[134:137], v[150:153], v[200:203], v[134:137]
	v_mfma_f32_16x16x32_f16 v[138:141], v[154:157], v[200:203], v[138:141]
	s_waitcnt lgkmcnt(0)
	v_mfma_f32_16x16x32_f16 v[2:5], v[146:149], v[204:207], v[2:5]
	v_mfma_f32_16x16x32_f16 v[6:9], v[150:153], v[204:207], v[6:9]
	v_mfma_f32_16x16x32_f16 v[10:13], v[154:157], v[204:207], v[10:13]
	v_mfma_f32_16x16x32_f16 v[14:17], v[158:161], v[204:207], v[14:17]
	v_mfma_f32_16x16x32_f16 v[142:145], v[158:161], v[200:203], v[142:145]
	s_setprio 0
	s_or_b32 s3, s49, s31
	s_lshl_b32 s0, s3, 12
	v_lshl_add_u64 v[158:159], v[166:167], 0, s[0:1]
	global_load_dwordx4 v[146:149], v[158:159], off
	global_load_dwordx4 v[150:153], v[158:159], off offset:1024
	global_load_dwordx4 v[154:157], v[158:159], off offset:2048
	s_nop 0
	global_load_dwordx4 v[158:161], v[158:159], off offset:3072
	v_lshl_add_u32 v208, s7, 10, v191
	ds_read_b128 v[192:195], v208
	ds_read_b128 v[196:199], v208 offset:16384
	ds_read_b128 v[200:203], v208 offset:32768
	ds_read_b128 v[204:207], v208 offset:49152
	s_setprio 1
	s_waitcnt vmcnt(11) lgkmcnt(3)
	v_mfma_f32_16x16x32_f16 v[34:37], v[18:21], v[192:195], v[34:37]
	s_waitcnt vmcnt(10)
	v_mfma_f32_16x16x32_f16 v[38:41], v[22:25], v[192:195], v[38:41]
	s_waitcnt vmcnt(9)
	v_mfma_f32_16x16x32_f16 v[42:45], v[26:29], v[192:195], v[42:45]
	s_waitcnt vmcnt(8)
	v_mfma_f32_16x16x32_f16 v[46:49], v[30:33], v[192:195], v[46:49]
	s_waitcnt lgkmcnt(2)
	v_mfma_f32_16x16x32_f16 v[50:53], v[18:21], v[196:199], v[50:53]
	v_mfma_f32_16x16x32_f16 v[54:57], v[22:25], v[196:199], v[54:57]
	v_mfma_f32_16x16x32_f16 v[58:61], v[26:29], v[196:199], v[58:61]
	v_mfma_f32_16x16x32_f16 v[62:65], v[30:33], v[196:199], v[62:65]
	s_waitcnt lgkmcnt(1)
	v_mfma_f32_16x16x32_f16 v[66:69], v[18:21], v[200:203], v[66:69]
	v_mfma_f32_16x16x32_f16 v[70:73], v[22:25], v[200:203], v[70:73]
	v_mfma_f32_16x16x32_f16 v[74:77], v[26:29], v[200:203], v[74:77]
	v_mfma_f32_16x16x32_f16 v[78:81], v[30:33], v[200:203], v[78:81]
	s_waitcnt lgkmcnt(0)
	v_mfma_f32_16x16x32_f16 v[82:85], v[18:21], v[204:207], v[82:85]
	v_mfma_f32_16x16x32_f16 v[86:89], v[22:25], v[204:207], v[86:89]
	v_mfma_f32_16x16x32_f16 v[90:93], v[26:29], v[204:207], v[90:93]
	v_mfma_f32_16x16x32_f16 v[94:97], v[30:33], v[204:207], v[94:97]
	s_setprio 0
	v_add_u32_e32 v192, 0x10000, v208
	v_add_u32_e32 v196, 0x14000, v208
	v_add_u32_e32 v200, 0x18000, v208
	v_add_u32_e32 v204, 0x1c000, v208
	ds_read_b128 v[192:195], v192
	ds_read_b128 v[196:199], v196
	ds_read_b128 v[200:203], v200
	ds_read_b128 v[204:207], v204
	s_setprio 1
	s_waitcnt lgkmcnt(3)
	v_mfma_f32_16x16x32_f16 v[98:101], v[18:21], v[192:195], v[98:101]
	v_mfma_f32_16x16x32_f16 v[102:105], v[22:25], v[192:195], v[102:105]
	v_mfma_f32_16x16x32_f16 v[106:109], v[26:29], v[192:195], v[106:109]
	v_mfma_f32_16x16x32_f16 v[110:113], v[30:33], v[192:195], v[110:113]
	s_waitcnt lgkmcnt(2)
	v_mfma_f32_16x16x32_f16 v[114:117], v[18:21], v[196:199], v[114:117]
	v_mfma_f32_16x16x32_f16 v[118:121], v[22:25], v[196:199], v[118:121]
	v_mfma_f32_16x16x32_f16 v[122:125], v[26:29], v[196:199], v[122:125]
	v_mfma_f32_16x16x32_f16 v[126:129], v[30:33], v[196:199], v[126:129]
	s_waitcnt lgkmcnt(1)
	v_mfma_f32_16x16x32_f16 v[130:133], v[18:21], v[200:203], v[130:133]
	v_mfma_f32_16x16x32_f16 v[134:137], v[22:25], v[200:203], v[134:137]
	v_mfma_f32_16x16x32_f16 v[138:141], v[26:29], v[200:203], v[138:141]
	s_waitcnt lgkmcnt(0)
	v_mfma_f32_16x16x32_f16 v[2:5], v[18:21], v[204:207], v[2:5]
	v_mfma_f32_16x16x32_f16 v[6:9], v[22:25], v[204:207], v[6:9]
	v_mfma_f32_16x16x32_f16 v[10:13], v[26:29], v[204:207], v[10:13]
	v_mfma_f32_16x16x32_f16 v[14:17], v[30:33], v[204:207], v[14:17]
	v_mfma_f32_16x16x32_f16 v[142:145], v[30:33], v[200:203], v[142:145]
	s_setprio 0
	s_or_b32 s7, s49, s48
	s_lshl_b32 s0, s7, 12
	v_lshl_add_u64 v[26:27], v[166:167], 0, s[0:1]
	global_load_dwordx4 v[18:21], v[26:27], off
	global_load_dwordx4 v[22:25], v[26:27], off offset:1024
	global_load_dwordx4 v[30:33], v[26:27], off offset:2048
	global_load_dwordx4 v[192:195], v[26:27], off offset:3072
	v_lshl_add_u32 v166, s2, 10, v191
	ds_read_b128 v[26:29], v166
	ds_read_b128 v[196:199], v166 offset:16384
	ds_read_b128 v[200:203], v166 offset:32768
	ds_read_b128 v[204:207], v166 offset:49152
	s_setprio 1
	s_waitcnt vmcnt(11) lgkmcnt(3)
	v_mfma_f32_16x16x32_f16 v[34:37], v[162:165], v[26:29], v[34:37]
	s_waitcnt vmcnt(10)
	v_mfma_f32_16x16x32_f16 v[38:41], v[168:171], v[26:29], v[38:41]
	s_waitcnt vmcnt(9)
	v_mfma_f32_16x16x32_f16 v[42:45], v[172:175], v[26:29], v[42:45]
	s_waitcnt vmcnt(8)
	v_mfma_f32_16x16x32_f16 v[26:29], v[176:179], v[26:29], v[46:49]
	s_waitcnt lgkmcnt(2)
	v_mfma_f32_16x16x32_f16 v[46:49], v[162:165], v[196:199], v[50:53]
	v_mfma_f32_16x16x32_f16 v[50:53], v[168:171], v[196:199], v[54:57]
	v_mfma_f32_16x16x32_f16 v[54:57], v[172:175], v[196:199], v[58:61]
	v_mfma_f32_16x16x32_f16 v[58:61], v[176:179], v[196:199], v[62:65]
	s_waitcnt lgkmcnt(1)
	v_mfma_f32_16x16x32_f16 v[62:65], v[162:165], v[200:203], v[66:69]
	v_mfma_f32_16x16x32_f16 v[66:69], v[168:171], v[200:203], v[70:73]
	v_mfma_f32_16x16x32_f16 v[70:73], v[172:175], v[200:203], v[74:77]
	v_mfma_f32_16x16x32_f16 v[74:77], v[176:179], v[200:203], v[78:81]
	s_waitcnt lgkmcnt(0)
	v_mfma_f32_16x16x32_f16 v[78:81], v[162:165], v[204:207], v[82:85]
	v_mfma_f32_16x16x32_f16 v[82:85], v[168:171], v[204:207], v[86:89]
	v_mfma_f32_16x16x32_f16 v[86:89], v[172:175], v[204:207], v[90:93]
	v_mfma_f32_16x16x32_f16 v[90:93], v[176:179], v[204:207], v[94:97]
	s_setprio 0
	s_nop 1
	v_add_u32_e32 v94, 0x10000, v166
	v_add_u32_e32 v167, 0x14000, v166
	ds_read_b128 v[94:97], v94
	ds_read_b128 v[196:199], v167
	v_add_u32_e32 v167, 0x18000, v166
	v_add_u32_e32 v166, 0x1c000, v166
	ds_read_b128 v[200:203], v167
	ds_read_b128 v[204:207], v166
	s_setprio 1
	s_waitcnt lgkmcnt(3)
	v_mfma_f32_16x16x32_f16 v[98:101], v[162:165], v[94:97], v[98:101]
	v_mfma_f32_16x16x32_f16 v[102:105], v[168:171], v[94:97], v[102:105]
	v_mfma_f32_16x16x32_f16 v[106:109], v[172:175], v[94:97], v[106:109]
	v_mfma_f32_16x16x32_f16 v[94:97], v[176:179], v[94:97], v[110:113]
	s_waitcnt lgkmcnt(2)
	v_mfma_f32_16x16x32_f16 v[110:113], v[162:165], v[196:199], v[114:117]
	v_mfma_f32_16x16x32_f16 v[114:117], v[168:171], v[196:199], v[118:121]
	v_mfma_f32_16x16x32_f16 v[118:121], v[172:175], v[196:199], v[122:125]
	v_mfma_f32_16x16x32_f16 v[122:125], v[176:179], v[196:199], v[126:129]
	s_waitcnt lgkmcnt(1)
	v_mfma_f32_16x16x32_f16 v[126:129], v[162:165], v[200:203], v[130:133]
	v_mfma_f32_16x16x32_f16 v[130:133], v[168:171], v[200:203], v[134:137]
	v_mfma_f32_16x16x32_f16 v[134:137], v[172:175], v[200:203], v[138:141]
	v_mfma_f32_16x16x32_f16 v[138:141], v[176:179], v[200:203], v[142:145]
	s_waitcnt lgkmcnt(0)
	v_mfma_f32_16x16x32_f16 v[2:5], v[162:165], v[204:207], v[2:5]
	v_mfma_f32_16x16x32_f16 v[6:9], v[168:171], v[204:207], v[6:9]
	v_mfma_f32_16x16x32_f16 v[10:13], v[172:175], v[204:207], v[10:13]
	v_mfma_f32_16x16x32_f16 v[14:17], v[176:179], v[204:207], v[14:17]
	s_setprio 0
	v_lshl_add_u32 v174, s3, 10, v191
	ds_read_b128 v[142:145], v174
	ds_read_b128 v[162:165], v174 offset:16384
	ds_read_b128 v[166:169], v174 offset:32768
	ds_read_b128 v[170:173], v174 offset:49152
	s_setprio 1
	s_waitcnt vmcnt(7) lgkmcnt(3)
	v_mfma_f32_16x16x32_f16 v[34:37], v[146:149], v[142:145], v[34:37]
	s_waitcnt vmcnt(6)
	v_mfma_f32_16x16x32_f16 v[38:41], v[150:153], v[142:145], v[38:41]
	s_waitcnt vmcnt(5)
	v_mfma_f32_16x16x32_f16 v[42:45], v[154:157], v[142:145], v[42:45]
	s_waitcnt vmcnt(4)
	v_mfma_f32_16x16x32_f16 v[26:29], v[158:161], v[142:145], v[26:29]
	s_waitcnt lgkmcnt(2)
	v_mfma_f32_16x16x32_f16 v[46:49], v[146:149], v[162:165], v[46:49]
	v_mfma_f32_16x16x32_f16 v[50:53], v[150:153], v[162:165], v[50:53]
	v_mfma_f32_16x16x32_f16 v[54:57], v[154:157], v[162:165], v[54:57]
	v_mfma_f32_16x16x32_f16 v[58:61], v[158:161], v[162:165], v[58:61]
	s_waitcnt lgkmcnt(1)
	v_mfma_f32_16x16x32_f16 v[62:65], v[146:149], v[166:169], v[62:65]
	v_mfma_f32_16x16x32_f16 v[66:69], v[150:153], v[166:169], v[66:69]
	v_mfma_f32_16x16x32_f16 v[70:73], v[154:157], v[166:169], v[70:73]
	v_mfma_f32_16x16x32_f16 v[74:77], v[158:161], v[166:169], v[74:77]
	s_waitcnt lgkmcnt(0)
	v_mfma_f32_16x16x32_f16 v[78:81], v[146:149], v[170:173], v[78:81]
	v_mfma_f32_16x16x32_f16 v[82:85], v[150:153], v[170:173], v[82:85]
	v_mfma_f32_16x16x32_f16 v[86:89], v[154:157], v[170:173], v[86:89]
	v_mfma_f32_16x16x32_f16 v[162:165], v[158:161], v[170:173], v[90:93]
	s_setprio 0
	s_nop 1
	v_add_u32_e32 v90, 0x10000, v174
	v_add_u32_e32 v142, 0x14000, v174
	v_add_u32_e32 v166, 0x18000, v174
	v_add_u32_e32 v170, 0x1c000, v174
	ds_read_b128 v[90:93], v90
	ds_read_b128 v[142:145], v142
	ds_read_b128 v[166:169], v166
	ds_read_b128 v[170:173], v170
	s_setprio 1
	s_waitcnt lgkmcnt(0)
	v_mfma_f32_16x16x32_f16 v[2:5], v[146:149], v[170:173], v[2:5]
	v_mfma_f32_16x16x32_f16 v[6:9], v[150:153], v[170:173], v[6:9]
	v_mfma_f32_16x16x32_f16 v[10:13], v[154:157], v[170:173], v[10:13]
	v_mfma_f32_16x16x32_f16 v[14:17], v[158:161], v[170:173], v[14:17]
	v_mfma_f32_16x16x32_f16 v[174:177], v[146:149], v[90:93], v[98:101]
	v_mfma_f32_16x16x32_f16 v[196:199], v[150:153], v[90:93], v[102:105]
	v_mfma_f32_16x16x32_f16 v[200:203], v[154:157], v[90:93], v[106:109]
	v_mfma_f32_16x16x32_f16 v[204:207], v[158:161], v[90:93], v[94:97]
	v_mfma_f32_16x16x32_f16 v[208:211], v[146:149], v[142:145], v[110:113]
	v_mfma_f32_16x16x32_f16 v[212:215], v[150:153], v[142:145], v[114:117]
	v_mfma_f32_16x16x32_f16 v[216:219], v[154:157], v[142:145], v[118:121]
	v_mfma_f32_16x16x32_f16 v[220:223], v[158:161], v[142:145], v[122:125]
	v_mfma_f32_16x16x32_f16 v[224:227], v[146:149], v[166:169], v[126:129]
	v_mfma_f32_16x16x32_f16 v[228:231], v[150:153], v[166:169], v[130:133]
	v_mfma_f32_16x16x32_f16 v[232:235], v[154:157], v[166:169], v[134:137]
	v_mfma_f32_16x16x32_f16 v[166:169], v[158:161], v[166:169], v[138:141]
	s_setprio 0
	v_lshl_add_u32 v158, s7, 10, v191
	ds_read_b128 v[90:93], v158
	ds_read_b128 v[94:97], v158 offset:16384
	ds_read_b128 v[98:101], v158 offset:32768
	ds_read_b128 v[146:149], v158 offset:49152
	s_setprio 1
	s_waitcnt vmcnt(3) lgkmcnt(3)
	v_mfma_f32_16x16x32_f16 v[150:153], v[18:21], v[90:93], v[34:37]
	s_waitcnt vmcnt(2)
	v_mfma_f32_16x16x32_f16 v[138:141], v[22:25], v[90:93], v[38:41]
	s_waitcnt vmcnt(1)
	v_mfma_f32_16x16x32_f16 v[154:157], v[30:33], v[90:93], v[42:45]
	s_waitcnt vmcnt(0)
	v_mfma_f32_16x16x32_f16 v[142:145], v[192:195], v[90:93], v[26:29]
	s_waitcnt lgkmcnt(2)
	v_mfma_f32_16x16x32_f16 v[134:137], v[18:21], v[94:97], v[46:49]
	v_mfma_f32_16x16x32_f16 v[122:125], v[22:25], v[94:97], v[50:53]
	v_mfma_f32_16x16x32_f16 v[130:133], v[30:33], v[94:97], v[54:57]
	v_mfma_f32_16x16x32_f16 v[126:129], v[192:195], v[94:97], v[58:61]
	s_waitcnt lgkmcnt(1)
	v_mfma_f32_16x16x32_f16 v[118:121], v[18:21], v[98:101], v[62:65]
	v_mfma_f32_16x16x32_f16 v[106:109], v[22:25], v[98:101], v[66:69]
	v_mfma_f32_16x16x32_f16 v[114:117], v[30:33], v[98:101], v[70:73]
	v_mfma_f32_16x16x32_f16 v[110:113], v[192:195], v[98:101], v[74:77]
	s_waitcnt lgkmcnt(0)
	v_mfma_f32_16x16x32_f16 v[102:105], v[18:21], v[146:149], v[78:81]
	v_mfma_f32_16x16x32_f16 v[90:93], v[22:25], v[146:149], v[82:85]
	v_mfma_f32_16x16x32_f16 v[98:101], v[30:33], v[146:149], v[86:89]
	v_mfma_f32_16x16x32_f16 v[94:97], v[192:195], v[146:149], v[162:165]
	s_setprio 0
	v_add_u32_e32 v26, 0x10000, v158
	v_add_u32_e32 v34, 0x14000, v158
	v_add_u32_e32 v38, 0x18000, v158
	ds_read_b128 v[26:29], v26
	ds_read_b128 v[34:37], v34
	v_add_u32_e32 v42, 0x1c000, v158
	ds_read_b128 v[38:41], v38
	ds_read_b128 v[146:149], v42
	s_setprio 1
	s_waitcnt lgkmcnt(3)
	v_mfma_f32_16x16x32_f16 v[86:89], v[18:21], v[26:29], v[174:177]
	v_mfma_f32_16x16x32_f16 v[74:77], v[22:25], v[26:29], v[196:199]
	v_mfma_f32_16x16x32_f16 v[82:85], v[30:33], v[26:29], v[200:203]
	v_mfma_f32_16x16x32_f16 v[78:81], v[192:195], v[26:29], v[204:207]
	s_waitcnt lgkmcnt(2)
	v_mfma_f32_16x16x32_f16 v[70:73], v[18:21], v[34:37], v[208:211]
	v_mfma_f32_16x16x32_f16 v[58:61], v[22:25], v[34:37], v[212:215]
	v_mfma_f32_16x16x32_f16 v[66:69], v[30:33], v[34:37], v[216:219]
	v_mfma_f32_16x16x32_f16 v[62:65], v[192:195], v[34:37], v[220:223]
	s_waitcnt lgkmcnt(1)
	v_mfma_f32_16x16x32_f16 v[54:57], v[18:21], v[38:41], v[224:227]
	v_mfma_f32_16x16x32_f16 v[42:45], v[22:25], v[38:41], v[228:231]
	v_mfma_f32_16x16x32_f16 v[50:53], v[30:33], v[38:41], v[232:235]
	v_mfma_f32_16x16x32_f16 v[46:49], v[192:195], v[38:41], v[166:169]
	s_waitcnt lgkmcnt(0)
	v_mfma_f32_16x16x32_f16 v[26:29], v[18:21], v[146:149], v[2:5]
	v_mfma_f32_16x16x32_f16 v[2:5], v[22:25], v[146:149], v[6:9]
	v_mfma_f32_16x16x32_f16 v[22:25], v[30:33], v[146:149], v[10:13]
	v_mfma_f32_16x16x32_f16 v[6:9], v[192:195], v[146:149], v[14:17]
	s_setprio 0
	s_lshl_b64 s[0:1], s[42:43], 2
	s_add_u32 s0, s18, s0
	s_addc_u32 s1, s19, s1
	s_lshl_b32 s2, s42, 8
	s_ashr_i32 s3, s2, 31
	v_lshlrev_b32_e32 v146, 5, v187
	s_lshl_b64 s[2:3], s[2:3], 2
	v_and_or_b32 v10, v190, 12, v146
	s_add_u32 s12, s12, s2
	s_addc_u32 s13, s13, s3
	v_lshlrev_b32_e32 v10, 2, v10
	v_add_u32_e32 v254, 0x22640, v10
	ds_read_b128 v[34:37], v254
	ds_read_b128 v[14:17], v254 offset:64
	ds_read_b128 v[38:41], v254 offset:1024
	ds_read_b128 v[18:21], v254 offset:1088
	ds_read_b128 v[30:33], v254 offset:2048
	ds_read_b128 v[10:13], v254 offset:2112
	s_add_u32 s12, s14, s2
	s_addc_u32 s13, s15, s3
	s_add_u32 s2, s16, s2
	s_addc_u32 s3, s17, s3
	s_nop 0
	v_cmp_gt_u32_e32 vcc, 16, v189
	s_mov_b32 s2, s69
	v_mov_b32_e32 v216, 0x3d38aa3b
	v_mov_b32_e32 v217, 0x3d38aa3b
	v_mov_b32_e32 v218, 0xbcb8aa3b
	v_mov_b32_e32 v219, 0xbcb8aa3b
	v_mov_b32_e32 v222, 1.0
	v_mov_b32_e32 v223, 1.0
	v_mov_b32_e32 v224, 0x4038aa3b
	v_mov_b32_e32 v225, 0x4038aa3b
	v_mov_b32_e32 v226, 0xbfb8aa3b
	v_mov_b32_e32 v227, 0xbfb8aa3b
	v_lshlrev_b32_e32 v232, 9, v187
	v_lshlrev_b32_e32 v233, 2, v188
	v_add3_u32 v232, s24, v232, v233
	s_waitcnt vmcnt(0) lgkmcnt(0)
	v_pk_mul_f32 v[34:35], v[34:35], v[224:225]
	v_pk_mul_f32 v[36:37], v[36:37], v[224:225]
	v_pk_mul_f32 v[14:15], v[14:15], v[224:225]
	v_pk_mul_f32 v[16:17], v[16:17], v[224:225]
	v_pk_mul_f32 v[38:39], v[38:39], v[226:227]
	v_pk_mul_f32 v[40:41], v[40:41], v[226:227]
	v_pk_mul_f32 v[18:19], v[18:19], v[226:227]
	v_pk_mul_f32 v[20:21], v[20:21], v[226:227]
	v_pk_fma_f32 v[150:151], v[150:151], v[216:217], v[34:35]
	v_pk_fma_f32 v[154:155], v[154:155], v[218:219], v[38:39]
	v_min_f32_e32 v150, 0x42700000, v150
	v_min_f32_e32 v151, 0x42700000, v151
	v_min_f32_e32 v154, 0x42700000, v154
	v_min_f32_e32 v155, 0x42700000, v155
	v_pk_fma_f32 v[152:153], v[152:153], v[216:217], v[36:37]
	v_pk_fma_f32 v[156:157], v[156:157], v[218:219], v[40:41]
	v_min_f32_e32 v152, 0x42700000, v152
	v_min_f32_e32 v153, 0x42700000, v153
	v_min_f32_e32 v156, 0x42700000, v156
	v_min_f32_e32 v157, 0x42700000, v157
	v_exp_f32_e32 v150, v150
	v_exp_f32_e32 v151, v151
	v_exp_f32_e32 v154, v154
	v_exp_f32_e32 v155, v155
	v_exp_f32_e32 v152, v152
	v_exp_f32_e32 v153, v153
	v_exp_f32_e32 v156, v156
	v_exp_f32_e32 v157, v157
	v_pk_fma_f32 v[228:229], v[150:151], v[30:31], v[30:31] neg_lo:[0,0,1] neg_hi:[0,0,1]
	v_pk_add_f32 v[154:155], v[154:155], v[222:223]
	v_pk_fma_f32 v[150:151], v[150:151], v[154:155], v[154:155]
	v_pk_fma_f32 v[230:231], v[152:153], v[32:33], v[32:33] neg_lo:[0,0,1] neg_hi:[0,0,1]
	v_pk_add_f32 v[156:157], v[156:157], v[222:223]
	v_pk_fma_f32 v[152:153], v[152:153], v[156:157], v[156:157]
	v_rcp_f32_e32 v150, v150
	v_rcp_f32_e32 v151, v151
	v_rcp_f32_e32 v152, v152
	v_rcp_f32_e32 v153, v153
	v_pk_mul_f32 v[200:201], v[228:229], v[150:151]
	v_pk_fma_f32 v[200:201], v[230:231], v[152:153], v[200:201]
	v_pk_fma_f32 v[138:139], v[138:139], v[216:217], v[14:15]
	v_pk_fma_f32 v[142:143], v[142:143], v[218:219], v[18:19]
	v_min_f32_e32 v138, 0x42700000, v138
	v_min_f32_e32 v139, 0x42700000, v139
	v_min_f32_e32 v142, 0x42700000, v142
	v_min_f32_e32 v143, 0x42700000, v143
	v_pk_fma_f32 v[140:141], v[140:141], v[216:217], v[16:17]
	v_pk_fma_f32 v[144:145], v[144:145], v[218:219], v[20:21]
	v_min_f32_e32 v140, 0x42700000, v140
	v_min_f32_e32 v141, 0x42700000, v141
	v_min_f32_e32 v144, 0x42700000, v144
	v_min_f32_e32 v145, 0x42700000, v145
	v_exp_f32_e32 v138, v138
	v_exp_f32_e32 v139, v139
	v_exp_f32_e32 v142, v142
	v_exp_f32_e32 v143, v143
	v_exp_f32_e32 v140, v140
	v_exp_f32_e32 v141, v141
	v_exp_f32_e32 v144, v144
	v_exp_f32_e32 v145, v145
	v_pk_fma_f32 v[228:229], v[138:139], v[10:11], v[10:11] neg_lo:[0,0,1] neg_hi:[0,0,1]
	v_pk_add_f32 v[142:143], v[142:143], v[222:223]
	v_pk_fma_f32 v[138:139], v[138:139], v[142:143], v[142:143]
	v_pk_fma_f32 v[230:231], v[140:141], v[12:13], v[12:13] neg_lo:[0,0,1] neg_hi:[0,0,1]
	v_pk_add_f32 v[144:145], v[144:145], v[222:223]
	v_pk_fma_f32 v[140:141], v[140:141], v[144:145], v[144:145]
	v_rcp_f32_e32 v138, v138
	v_rcp_f32_e32 v139, v139
	v_rcp_f32_e32 v140, v140
	v_rcp_f32_e32 v141, v141
	v_pk_fma_f32 v[200:201], v[228:229], v[138:139], v[200:201]
	v_pk_fma_f32 v[200:201], v[230:231], v[140:141], v[200:201]
	v_pk_fma_f32 v[134:135], v[134:135], v[216:217], v[34:35]
	v_pk_fma_f32 v[130:131], v[130:131], v[218:219], v[38:39]
	v_min_f32_e32 v134, 0x42700000, v134
	v_min_f32_e32 v135, 0x42700000, v135
	v_min_f32_e32 v130, 0x42700000, v130
	v_min_f32_e32 v131, 0x42700000, v131
	v_pk_fma_f32 v[136:137], v[136:137], v[216:217], v[36:37]
	v_pk_fma_f32 v[132:133], v[132:133], v[218:219], v[40:41]
	v_min_f32_e32 v136, 0x42700000, v136
	v_min_f32_e32 v137, 0x42700000, v137
	v_min_f32_e32 v132, 0x42700000, v132
	v_min_f32_e32 v133, 0x42700000, v133
	v_exp_f32_e32 v134, v134
	v_exp_f32_e32 v135, v135
	v_exp_f32_e32 v130, v130
	v_exp_f32_e32 v131, v131
	v_exp_f32_e32 v136, v136
	v_exp_f32_e32 v137, v137
	v_exp_f32_e32 v132, v132
	v_exp_f32_e32 v133, v133
	v_pk_fma_f32 v[228:229], v[134:135], v[30:31], v[30:31] neg_lo:[0,0,1] neg_hi:[0,0,1]
	v_pk_add_f32 v[130:131], v[130:131], v[222:223]
	v_pk_fma_f32 v[134:135], v[134:135], v[130:131], v[130:131]
	v_pk_fma_f32 v[230:231], v[136:137], v[32:33], v[32:33] neg_lo:[0,0,1] neg_hi:[0,0,1]
	v_pk_add_f32 v[132:133], v[132:133], v[222:223]
	v_pk_fma_f32 v[136:137], v[136:137], v[132:133], v[132:133]
	v_rcp_f32_e32 v134, v134
	v_rcp_f32_e32 v135, v135
	v_rcp_f32_e32 v136, v136
	v_rcp_f32_e32 v137, v137
	v_pk_mul_f32 v[202:203], v[228:229], v[134:135]
	v_pk_fma_f32 v[202:203], v[230:231], v[136:137], v[202:203]
	v_pk_fma_f32 v[122:123], v[122:123], v[216:217], v[14:15]
	v_pk_fma_f32 v[126:127], v[126:127], v[218:219], v[18:19]
	v_min_f32_e32 v122, 0x42700000, v122
	v_min_f32_e32 v123, 0x42700000, v123
	v_min_f32_e32 v126, 0x42700000, v126
	v_min_f32_e32 v127, 0x42700000, v127
	v_pk_fma_f32 v[124:125], v[124:125], v[216:217], v[16:17]
	v_pk_fma_f32 v[128:129], v[128:129], v[218:219], v[20:21]
	v_min_f32_e32 v124, 0x42700000, v124
	v_min_f32_e32 v125, 0x42700000, v125
	v_min_f32_e32 v128, 0x42700000, v128
	v_min_f32_e32 v129, 0x42700000, v129
	v_exp_f32_e32 v122, v122
	v_exp_f32_e32 v123, v123
	v_exp_f32_e32 v126, v126
	v_exp_f32_e32 v127, v127
	v_exp_f32_e32 v124, v124
	v_exp_f32_e32 v125, v125
	v_exp_f32_e32 v128, v128
	v_exp_f32_e32 v129, v129
	v_pk_fma_f32 v[228:229], v[122:123], v[10:11], v[10:11] neg_lo:[0,0,1] neg_hi:[0,0,1]
	v_pk_add_f32 v[126:127], v[126:127], v[222:223]
	v_pk_fma_f32 v[122:123], v[122:123], v[126:127], v[126:127]
	v_pk_fma_f32 v[230:231], v[124:125], v[12:13], v[12:13] neg_lo:[0,0,1] neg_hi:[0,0,1]
	v_pk_add_f32 v[128:129], v[128:129], v[222:223]
	v_pk_fma_f32 v[124:125], v[124:125], v[128:129], v[128:129]
	v_rcp_f32_e32 v122, v122
	v_rcp_f32_e32 v123, v123
	v_rcp_f32_e32 v124, v124
	v_rcp_f32_e32 v125, v125
	v_pk_fma_f32 v[202:203], v[228:229], v[122:123], v[202:203]
	v_pk_fma_f32 v[202:203], v[230:231], v[124:125], v[202:203]
	v_pk_fma_f32 v[118:119], v[118:119], v[216:217], v[34:35]
	v_pk_fma_f32 v[114:115], v[114:115], v[218:219], v[38:39]
	v_min_f32_e32 v118, 0x42700000, v118
	v_min_f32_e32 v119, 0x42700000, v119
	v_min_f32_e32 v114, 0x42700000, v114
	v_min_f32_e32 v115, 0x42700000, v115
	v_pk_fma_f32 v[120:121], v[120:121], v[216:217], v[36:37]
	v_pk_fma_f32 v[116:117], v[116:117], v[218:219], v[40:41]
	v_min_f32_e32 v120, 0x42700000, v120
	v_min_f32_e32 v121, 0x42700000, v121
	v_min_f32_e32 v116, 0x42700000, v116
	v_min_f32_e32 v117, 0x42700000, v117
	v_exp_f32_e32 v118, v118
	v_exp_f32_e32 v119, v119
	v_exp_f32_e32 v114, v114
	v_exp_f32_e32 v115, v115
	v_exp_f32_e32 v120, v120
	v_exp_f32_e32 v121, v121
	v_exp_f32_e32 v116, v116
	v_exp_f32_e32 v117, v117
	v_pk_fma_f32 v[228:229], v[118:119], v[30:31], v[30:31] neg_lo:[0,0,1] neg_hi:[0,0,1]
	v_pk_add_f32 v[114:115], v[114:115], v[222:223]
	v_pk_fma_f32 v[118:119], v[118:119], v[114:115], v[114:115]
	v_pk_fma_f32 v[230:231], v[120:121], v[32:33], v[32:33] neg_lo:[0,0,1] neg_hi:[0,0,1]
	v_pk_add_f32 v[116:117], v[116:117], v[222:223]
	v_pk_fma_f32 v[120:121], v[120:121], v[116:117], v[116:117]
	v_rcp_f32_e32 v118, v118
	v_rcp_f32_e32 v119, v119
	v_rcp_f32_e32 v120, v120
	v_rcp_f32_e32 v121, v121
	v_pk_mul_f32 v[204:205], v[228:229], v[118:119]
	v_pk_fma_f32 v[204:205], v[230:231], v[120:121], v[204:205]
	v_pk_fma_f32 v[106:107], v[106:107], v[216:217], v[14:15]
	v_pk_fma_f32 v[110:111], v[110:111], v[218:219], v[18:19]
	v_min_f32_e32 v106, 0x42700000, v106
	v_min_f32_e32 v107, 0x42700000, v107
	v_min_f32_e32 v110, 0x42700000, v110
	v_min_f32_e32 v111, 0x42700000, v111
	v_pk_fma_f32 v[108:109], v[108:109], v[216:217], v[16:17]
	v_pk_fma_f32 v[112:113], v[112:113], v[218:219], v[20:21]
	v_min_f32_e32 v108, 0x42700000, v108
	v_min_f32_e32 v109, 0x42700000, v109
	v_min_f32_e32 v112, 0x42700000, v112
	v_min_f32_e32 v113, 0x42700000, v113
	v_exp_f32_e32 v106, v106
	v_exp_f32_e32 v107, v107
	v_exp_f32_e32 v110, v110
	v_exp_f32_e32 v111, v111
	v_exp_f32_e32 v108, v108
	v_exp_f32_e32 v109, v109
	v_exp_f32_e32 v112, v112
	v_exp_f32_e32 v113, v113
	v_pk_fma_f32 v[228:229], v[106:107], v[10:11], v[10:11] neg_lo:[0,0,1] neg_hi:[0,0,1]
	v_pk_add_f32 v[110:111], v[110:111], v[222:223]
	v_pk_fma_f32 v[106:107], v[106:107], v[110:111], v[110:111]
	v_pk_fma_f32 v[230:231], v[108:109], v[12:13], v[12:13] neg_lo:[0,0,1] neg_hi:[0,0,1]
	v_pk_add_f32 v[112:113], v[112:113], v[222:223]
	v_pk_fma_f32 v[108:109], v[108:109], v[112:113], v[112:113]
	v_rcp_f32_e32 v106, v106
	v_rcp_f32_e32 v107, v107
	v_rcp_f32_e32 v108, v108
	v_rcp_f32_e32 v109, v109
	v_pk_fma_f32 v[204:205], v[228:229], v[106:107], v[204:205]
	v_pk_fma_f32 v[204:205], v[230:231], v[108:109], v[204:205]
	v_pk_fma_f32 v[102:103], v[102:103], v[216:217], v[34:35]
	v_pk_fma_f32 v[98:99], v[98:99], v[218:219], v[38:39]
	v_min_f32_e32 v102, 0x42700000, v102
	v_min_f32_e32 v103, 0x42700000, v103
	v_min_f32_e32 v98, 0x42700000, v98
	v_min_f32_e32 v99, 0x42700000, v99
	v_pk_fma_f32 v[104:105], v[104:105], v[216:217], v[36:37]
	v_pk_fma_f32 v[100:101], v[100:101], v[218:219], v[40:41]
	v_min_f32_e32 v104, 0x42700000, v104
	v_min_f32_e32 v105, 0x42700000, v105
	v_min_f32_e32 v100, 0x42700000, v100
	v_min_f32_e32 v101, 0x42700000, v101
	v_exp_f32_e32 v102, v102
	v_exp_f32_e32 v103, v103
	v_exp_f32_e32 v98, v98
	v_exp_f32_e32 v99, v99
	v_exp_f32_e32 v104, v104
	v_exp_f32_e32 v105, v105
	v_exp_f32_e32 v100, v100
	v_exp_f32_e32 v101, v101
	v_pk_fma_f32 v[228:229], v[102:103], v[30:31], v[30:31] neg_lo:[0,0,1] neg_hi:[0,0,1]
	v_pk_add_f32 v[98:99], v[98:99], v[222:223]
	v_pk_fma_f32 v[102:103], v[102:103], v[98:99], v[98:99]
	v_pk_fma_f32 v[230:231], v[104:105], v[32:33], v[32:33] neg_lo:[0,0,1] neg_hi:[0,0,1]
	v_pk_add_f32 v[100:101], v[100:101], v[222:223]
	v_pk_fma_f32 v[104:105], v[104:105], v[100:101], v[100:101]
	v_rcp_f32_e32 v102, v102
	v_rcp_f32_e32 v103, v103
	v_rcp_f32_e32 v104, v104
	v_rcp_f32_e32 v105, v105
	v_pk_mul_f32 v[206:207], v[228:229], v[102:103]
	v_pk_fma_f32 v[206:207], v[230:231], v[104:105], v[206:207]
	v_pk_fma_f32 v[90:91], v[90:91], v[216:217], v[14:15]
	v_pk_fma_f32 v[94:95], v[94:95], v[218:219], v[18:19]
	v_min_f32_e32 v90, 0x42700000, v90
	v_min_f32_e32 v91, 0x42700000, v91
	v_min_f32_e32 v94, 0x42700000, v94
	v_min_f32_e32 v95, 0x42700000, v95
	v_pk_fma_f32 v[92:93], v[92:93], v[216:217], v[16:17]
	v_pk_fma_f32 v[96:97], v[96:97], v[218:219], v[20:21]
	v_min_f32_e32 v92, 0x42700000, v92
	v_min_f32_e32 v93, 0x42700000, v93
	v_min_f32_e32 v96, 0x42700000, v96
	v_min_f32_e32 v97, 0x42700000, v97
	v_exp_f32_e32 v90, v90
	v_exp_f32_e32 v91, v91
	v_exp_f32_e32 v94, v94
	v_exp_f32_e32 v95, v95
	v_exp_f32_e32 v92, v92
	v_exp_f32_e32 v93, v93
	v_exp_f32_e32 v96, v96
	v_exp_f32_e32 v97, v97
	v_pk_fma_f32 v[228:229], v[90:91], v[10:11], v[10:11] neg_lo:[0,0,1] neg_hi:[0,0,1]
	v_pk_add_f32 v[94:95], v[94:95], v[222:223]
	v_pk_fma_f32 v[90:91], v[90:91], v[94:95], v[94:95]
	v_pk_fma_f32 v[230:231], v[92:93], v[12:13], v[12:13] neg_lo:[0,0,1] neg_hi:[0,0,1]
	v_pk_add_f32 v[96:97], v[96:97], v[222:223]
	v_pk_fma_f32 v[92:93], v[92:93], v[96:97], v[96:97]
	v_rcp_f32_e32 v90, v90
	v_rcp_f32_e32 v91, v91
	v_rcp_f32_e32 v92, v92
	v_rcp_f32_e32 v93, v93
	v_pk_fma_f32 v[206:207], v[228:229], v[90:91], v[206:207]
	v_pk_fma_f32 v[206:207], v[230:231], v[92:93], v[206:207]
	v_pk_fma_f32 v[86:87], v[86:87], v[216:217], v[34:35]
	v_pk_fma_f32 v[82:83], v[82:83], v[218:219], v[38:39]
	v_min_f32_e32 v86, 0x42700000, v86
	v_min_f32_e32 v87, 0x42700000, v87
	v_min_f32_e32 v82, 0x42700000, v82
	v_min_f32_e32 v83, 0x42700000, v83
	v_pk_fma_f32 v[88:89], v[88:89], v[216:217], v[36:37]
	v_pk_fma_f32 v[84:85], v[84:85], v[218:219], v[40:41]
	v_min_f32_e32 v88, 0x42700000, v88
	v_min_f32_e32 v89, 0x42700000, v89
	v_min_f32_e32 v84, 0x42700000, v84
	v_min_f32_e32 v85, 0x42700000, v85
	v_exp_f32_e32 v86, v86
	v_exp_f32_e32 v87, v87
	v_exp_f32_e32 v82, v82
	v_exp_f32_e32 v83, v83
	v_exp_f32_e32 v88, v88
	v_exp_f32_e32 v89, v89
	v_exp_f32_e32 v84, v84
	v_exp_f32_e32 v85, v85
	v_pk_fma_f32 v[228:229], v[86:87], v[30:31], v[30:31] neg_lo:[0,0,1] neg_hi:[0,0,1]
	v_pk_add_f32 v[82:83], v[82:83], v[222:223]
	v_pk_fma_f32 v[86:87], v[86:87], v[82:83], v[82:83]
	v_pk_fma_f32 v[230:231], v[88:89], v[32:33], v[32:33] neg_lo:[0,0,1] neg_hi:[0,0,1]
	v_pk_add_f32 v[84:85], v[84:85], v[222:223]
	v_pk_fma_f32 v[88:89], v[88:89], v[84:85], v[84:85]
	v_rcp_f32_e32 v86, v86
	v_rcp_f32_e32 v87, v87
	v_rcp_f32_e32 v88, v88
	v_rcp_f32_e32 v89, v89
	v_pk_mul_f32 v[208:209], v[228:229], v[86:87]
	v_pk_fma_f32 v[208:209], v[230:231], v[88:89], v[208:209]
	v_pk_fma_f32 v[74:75], v[74:75], v[216:217], v[14:15]
	v_pk_fma_f32 v[78:79], v[78:79], v[218:219], v[18:19]
	v_min_f32_e32 v74, 0x42700000, v74
	v_min_f32_e32 v75, 0x42700000, v75
	v_min_f32_e32 v78, 0x42700000, v78
	v_min_f32_e32 v79, 0x42700000, v79
	v_pk_fma_f32 v[76:77], v[76:77], v[216:217], v[16:17]
	v_pk_fma_f32 v[80:81], v[80:81], v[218:219], v[20:21]
	v_min_f32_e32 v76, 0x42700000, v76
	v_min_f32_e32 v77, 0x42700000, v77
	v_min_f32_e32 v80, 0x42700000, v80
	v_min_f32_e32 v81, 0x42700000, v81
	v_exp_f32_e32 v74, v74
	v_exp_f32_e32 v75, v75
	v_exp_f32_e32 v78, v78
	v_exp_f32_e32 v79, v79
	v_exp_f32_e32 v76, v76
	v_exp_f32_e32 v77, v77
	v_exp_f32_e32 v80, v80
	v_exp_f32_e32 v81, v81
	v_pk_fma_f32 v[228:229], v[74:75], v[10:11], v[10:11] neg_lo:[0,0,1] neg_hi:[0,0,1]
	v_pk_add_f32 v[78:79], v[78:79], v[222:223]
	v_pk_fma_f32 v[74:75], v[74:75], v[78:79], v[78:79]
	v_pk_fma_f32 v[230:231], v[76:77], v[12:13], v[12:13] neg_lo:[0,0,1] neg_hi:[0,0,1]
	v_pk_add_f32 v[80:81], v[80:81], v[222:223]
	v_pk_fma_f32 v[76:77], v[76:77], v[80:81], v[80:81]
	v_rcp_f32_e32 v74, v74
	v_rcp_f32_e32 v75, v75
	v_rcp_f32_e32 v76, v76
	v_rcp_f32_e32 v77, v77
	v_pk_fma_f32 v[208:209], v[228:229], v[74:75], v[208:209]
	v_pk_fma_f32 v[208:209], v[230:231], v[76:77], v[208:209]
	v_pk_fma_f32 v[70:71], v[70:71], v[216:217], v[34:35]
	v_pk_fma_f32 v[66:67], v[66:67], v[218:219], v[38:39]
	v_min_f32_e32 v70, 0x42700000, v70
	v_min_f32_e32 v71, 0x42700000, v71
	v_min_f32_e32 v66, 0x42700000, v66
	v_min_f32_e32 v67, 0x42700000, v67
	v_pk_fma_f32 v[72:73], v[72:73], v[216:217], v[36:37]
	v_pk_fma_f32 v[68:69], v[68:69], v[218:219], v[40:41]
	v_min_f32_e32 v72, 0x42700000, v72
	v_min_f32_e32 v73, 0x42700000, v73
	v_min_f32_e32 v68, 0x42700000, v68
	v_min_f32_e32 v69, 0x42700000, v69
	v_exp_f32_e32 v70, v70
	v_exp_f32_e32 v71, v71
	v_exp_f32_e32 v66, v66
	v_exp_f32_e32 v67, v67
	v_exp_f32_e32 v72, v72
	v_exp_f32_e32 v73, v73
	v_exp_f32_e32 v68, v68
	v_exp_f32_e32 v69, v69
	v_pk_fma_f32 v[228:229], v[70:71], v[30:31], v[30:31] neg_lo:[0,0,1] neg_hi:[0,0,1]
	v_pk_add_f32 v[66:67], v[66:67], v[222:223]
	v_pk_fma_f32 v[70:71], v[70:71], v[66:67], v[66:67]
	v_pk_fma_f32 v[230:231], v[72:73], v[32:33], v[32:33] neg_lo:[0,0,1] neg_hi:[0,0,1]
	v_pk_add_f32 v[68:69], v[68:69], v[222:223]
	v_pk_fma_f32 v[72:73], v[72:73], v[68:69], v[68:69]
	v_rcp_f32_e32 v70, v70
	v_rcp_f32_e32 v71, v71
	v_rcp_f32_e32 v72, v72
	v_rcp_f32_e32 v73, v73
	v_pk_mul_f32 v[210:211], v[228:229], v[70:71]
	v_pk_fma_f32 v[210:211], v[230:231], v[72:73], v[210:211]
	v_pk_fma_f32 v[58:59], v[58:59], v[216:217], v[14:15]
	v_pk_fma_f32 v[62:63], v[62:63], v[218:219], v[18:19]
	v_min_f32_e32 v58, 0x42700000, v58
	v_min_f32_e32 v59, 0x42700000, v59
	v_min_f32_e32 v62, 0x42700000, v62
	v_min_f32_e32 v63, 0x42700000, v63
	v_pk_fma_f32 v[60:61], v[60:61], v[216:217], v[16:17]
	v_pk_fma_f32 v[64:65], v[64:65], v[218:219], v[20:21]
	v_min_f32_e32 v60, 0x42700000, v60
	v_min_f32_e32 v61, 0x42700000, v61
	v_min_f32_e32 v64, 0x42700000, v64
	v_min_f32_e32 v65, 0x42700000, v65
	v_exp_f32_e32 v58, v58
	v_exp_f32_e32 v59, v59
	v_exp_f32_e32 v62, v62
	v_exp_f32_e32 v63, v63
	v_exp_f32_e32 v60, v60
	v_exp_f32_e32 v61, v61
	v_exp_f32_e32 v64, v64
	v_exp_f32_e32 v65, v65
	v_pk_fma_f32 v[228:229], v[58:59], v[10:11], v[10:11] neg_lo:[0,0,1] neg_hi:[0,0,1]
	v_pk_add_f32 v[62:63], v[62:63], v[222:223]
	v_pk_fma_f32 v[58:59], v[58:59], v[62:63], v[62:63]
	v_pk_fma_f32 v[230:231], v[60:61], v[12:13], v[12:13] neg_lo:[0,0,1] neg_hi:[0,0,1]
	v_pk_add_f32 v[64:65], v[64:65], v[222:223]
	v_pk_fma_f32 v[60:61], v[60:61], v[64:65], v[64:65]
	v_rcp_f32_e32 v58, v58
	v_rcp_f32_e32 v59, v59
	v_rcp_f32_e32 v60, v60
	v_rcp_f32_e32 v61, v61
	v_pk_fma_f32 v[210:211], v[228:229], v[58:59], v[210:211]
	v_pk_fma_f32 v[210:211], v[230:231], v[60:61], v[210:211]
	v_pk_fma_f32 v[54:55], v[54:55], v[216:217], v[34:35]
	v_pk_fma_f32 v[50:51], v[50:51], v[218:219], v[38:39]
	v_min_f32_e32 v54, 0x42700000, v54
	v_min_f32_e32 v55, 0x42700000, v55
	v_min_f32_e32 v50, 0x42700000, v50
	v_min_f32_e32 v51, 0x42700000, v51
	v_pk_fma_f32 v[56:57], v[56:57], v[216:217], v[36:37]
	v_pk_fma_f32 v[52:53], v[52:53], v[218:219], v[40:41]
	v_min_f32_e32 v56, 0x42700000, v56
	v_min_f32_e32 v57, 0x42700000, v57
	v_min_f32_e32 v52, 0x42700000, v52
	v_min_f32_e32 v53, 0x42700000, v53
	v_exp_f32_e32 v54, v54
	v_exp_f32_e32 v55, v55
	v_exp_f32_e32 v50, v50
	v_exp_f32_e32 v51, v51
	v_exp_f32_e32 v56, v56
	v_exp_f32_e32 v57, v57
	v_exp_f32_e32 v52, v52
	v_exp_f32_e32 v53, v53
	v_pk_fma_f32 v[228:229], v[54:55], v[30:31], v[30:31] neg_lo:[0,0,1] neg_hi:[0,0,1]
	v_pk_add_f32 v[50:51], v[50:51], v[222:223]
	v_pk_fma_f32 v[54:55], v[54:55], v[50:51], v[50:51]
	v_pk_fma_f32 v[230:231], v[56:57], v[32:33], v[32:33] neg_lo:[0,0,1] neg_hi:[0,0,1]
	v_pk_add_f32 v[52:53], v[52:53], v[222:223]
	v_pk_fma_f32 v[56:57], v[56:57], v[52:53], v[52:53]
	v_rcp_f32_e32 v54, v54
	v_rcp_f32_e32 v55, v55
	v_rcp_f32_e32 v56, v56
	v_rcp_f32_e32 v57, v57
	v_pk_mul_f32 v[212:213], v[228:229], v[54:55]
	v_pk_fma_f32 v[212:213], v[230:231], v[56:57], v[212:213]
	v_pk_fma_f32 v[42:43], v[42:43], v[216:217], v[14:15]
	v_pk_fma_f32 v[46:47], v[46:47], v[218:219], v[18:19]
	v_min_f32_e32 v42, 0x42700000, v42
	v_min_f32_e32 v43, 0x42700000, v43
	v_min_f32_e32 v46, 0x42700000, v46
	v_min_f32_e32 v47, 0x42700000, v47
	v_pk_fma_f32 v[44:45], v[44:45], v[216:217], v[16:17]
	v_pk_fma_f32 v[48:49], v[48:49], v[218:219], v[20:21]
	v_min_f32_e32 v44, 0x42700000, v44
	v_min_f32_e32 v45, 0x42700000, v45
	v_min_f32_e32 v48, 0x42700000, v48
	v_min_f32_e32 v49, 0x42700000, v49
	v_exp_f32_e32 v42, v42
	v_exp_f32_e32 v43, v43
	v_exp_f32_e32 v46, v46
	v_exp_f32_e32 v47, v47
	v_exp_f32_e32 v44, v44
	v_exp_f32_e32 v45, v45
	v_exp_f32_e32 v48, v48
	v_exp_f32_e32 v49, v49
	v_pk_fma_f32 v[228:229], v[42:43], v[10:11], v[10:11] neg_lo:[0,0,1] neg_hi:[0,0,1]
	v_pk_add_f32 v[46:47], v[46:47], v[222:223]
	v_pk_fma_f32 v[42:43], v[42:43], v[46:47], v[46:47]
	v_pk_fma_f32 v[230:231], v[44:45], v[12:13], v[12:13] neg_lo:[0,0,1] neg_hi:[0,0,1]
	v_pk_add_f32 v[48:49], v[48:49], v[222:223]
	v_pk_fma_f32 v[44:45], v[44:45], v[48:49], v[48:49]
	v_rcp_f32_e32 v42, v42
	v_rcp_f32_e32 v43, v43
	v_rcp_f32_e32 v44, v44
	v_rcp_f32_e32 v45, v45
	v_pk_fma_f32 v[212:213], v[228:229], v[42:43], v[212:213]
	v_pk_fma_f32 v[212:213], v[230:231], v[44:45], v[212:213]
	v_pk_fma_f32 v[26:27], v[26:27], v[216:217], v[34:35]
	v_pk_fma_f32 v[22:23], v[22:23], v[218:219], v[38:39]
	v_min_f32_e32 v26, 0x42700000, v26
	v_min_f32_e32 v27, 0x42700000, v27
	v_min_f32_e32 v22, 0x42700000, v22
	v_min_f32_e32 v23, 0x42700000, v23
	v_pk_fma_f32 v[28:29], v[28:29], v[216:217], v[36:37]
	v_pk_fma_f32 v[24:25], v[24:25], v[218:219], v[40:41]
	v_min_f32_e32 v28, 0x42700000, v28
	v_min_f32_e32 v29, 0x42700000, v29
	v_min_f32_e32 v24, 0x42700000, v24
	v_min_f32_e32 v25, 0x42700000, v25
	v_exp_f32_e32 v26, v26
	v_exp_f32_e32 v27, v27
	v_exp_f32_e32 v22, v22
	v_exp_f32_e32 v23, v23
	v_exp_f32_e32 v28, v28
	v_exp_f32_e32 v29, v29
	v_exp_f32_e32 v24, v24
	v_exp_f32_e32 v25, v25
	v_pk_fma_f32 v[228:229], v[26:27], v[30:31], v[30:31] neg_lo:[0,0,1] neg_hi:[0,0,1]
	v_pk_add_f32 v[22:23], v[22:23], v[222:223]
	v_pk_fma_f32 v[26:27], v[26:27], v[22:23], v[22:23]
	v_pk_fma_f32 v[230:231], v[28:29], v[32:33], v[32:33] neg_lo:[0,0,1] neg_hi:[0,0,1]
	v_pk_add_f32 v[24:25], v[24:25], v[222:223]
	v_pk_fma_f32 v[28:29], v[28:29], v[24:25], v[24:25]
	v_rcp_f32_e32 v26, v26
	v_rcp_f32_e32 v27, v27
	v_rcp_f32_e32 v28, v28
	v_rcp_f32_e32 v29, v29
	v_pk_mul_f32 v[214:215], v[228:229], v[26:27]
	v_pk_fma_f32 v[214:215], v[230:231], v[28:29], v[214:215]
	v_pk_fma_f32 v[2:3], v[2:3], v[216:217], v[14:15]
	v_pk_fma_f32 v[6:7], v[6:7], v[218:219], v[18:19]
	v_min_f32_e32 v2, 0x42700000, v2
	v_min_f32_e32 v3, 0x42700000, v3
	v_min_f32_e32 v6, 0x42700000, v6
	v_min_f32_e32 v7, 0x42700000, v7
	v_pk_fma_f32 v[4:5], v[4:5], v[216:217], v[16:17]
	v_pk_fma_f32 v[8:9], v[8:9], v[218:219], v[20:21]
	v_min_f32_e32 v4, 0x42700000, v4
	v_min_f32_e32 v5, 0x42700000, v5
	v_min_f32_e32 v8, 0x42700000, v8
	v_min_f32_e32 v9, 0x42700000, v9
	v_exp_f32_e32 v2, v2
	v_exp_f32_e32 v3, v3
	v_exp_f32_e32 v6, v6
	v_exp_f32_e32 v7, v7
	v_exp_f32_e32 v4, v4
	v_exp_f32_e32 v5, v5
	v_exp_f32_e32 v8, v8
	v_exp_f32_e32 v9, v9
	v_pk_fma_f32 v[228:229], v[2:3], v[10:11], v[10:11] neg_lo:[0,0,1] neg_hi:[0,0,1]
	v_pk_add_f32 v[6:7], v[6:7], v[222:223]
	v_pk_fma_f32 v[2:3], v[2:3], v[6:7], v[6:7]
	v_pk_fma_f32 v[230:231], v[4:5], v[12:13], v[12:13] neg_lo:[0,0,1] neg_hi:[0,0,1]
	v_pk_add_f32 v[8:9], v[8:9], v[222:223]
	v_pk_fma_f32 v[4:5], v[4:5], v[8:9], v[8:9]
	v_rcp_f32_e32 v2, v2
	v_rcp_f32_e32 v3, v3
	v_rcp_f32_e32 v4, v4
	v_rcp_f32_e32 v5, v5
	v_pk_fma_f32 v[214:215], v[228:229], v[2:3], v[214:215]
	v_pk_fma_f32 v[214:215], v[230:231], v[4:5], v[214:215]
	v_add_f32_e32 v240, v200, v201
	v_add_f32_e32 v241, v202, v203
	v_add_f32_e32 v242, v204, v205
	v_add_f32_e32 v243, v206, v207
	v_add_f32_e32 v244, v208, v209
	v_add_f32_e32 v245, v210, v211
	v_add_f32_e32 v246, v212, v213
	v_add_f32_e32 v247, v214, v215
	ds_bpermute_b32 v200, v181, v240
	ds_bpermute_b32 v201, v181, v241
	ds_bpermute_b32 v202, v181, v242
	ds_bpermute_b32 v203, v181, v243
	ds_bpermute_b32 v204, v181, v244
	ds_bpermute_b32 v205, v181, v245
	ds_bpermute_b32 v206, v181, v246
	ds_bpermute_b32 v207, v181, v247
	s_waitcnt lgkmcnt(0)
	v_add_f32_e32 v240, v240, v200
	v_add_f32_e32 v241, v241, v201
	v_add_f32_e32 v242, v242, v202
	v_add_f32_e32 v243, v243, v203
	v_add_f32_e32 v244, v244, v204
	v_add_f32_e32 v245, v245, v205
	v_add_f32_e32 v246, v246, v206
	v_add_f32_e32 v247, v247, v207
	ds_bpermute_b32 v200, v183, v240
	ds_bpermute_b32 v201, v183, v241
	ds_bpermute_b32 v202, v183, v242
	ds_bpermute_b32 v203, v183, v243
	ds_bpermute_b32 v204, v183, v244
	ds_bpermute_b32 v205, v183, v245
	ds_bpermute_b32 v206, v183, v246
	ds_bpermute_b32 v207, v183, v247
	s_waitcnt lgkmcnt(0)
	v_add_f32_e32 v240, v240, v200
	v_add_f32_e32 v241, v241, v201
	v_add_f32_e32 v242, v242, v202
	v_add_f32_e32 v243, v243, v203
	v_add_f32_e32 v244, v244, v204
	v_add_f32_e32 v245, v245, v205
	v_add_f32_e32 v246, v246, v206
	v_add_f32_e32 v247, v247, v207
	s_and_saveexec_b64 s[64:65], vcc
	ds_write2_b32 v232, v240, v241 offset0:0 offset1:16
	ds_write2_b32 v232, v242, v243 offset0:32 offset1:48
	ds_write2_b32 v232, v244, v245 offset0:64 offset1:80
	ds_write2_b32 v232, v246, v247 offset0:96 offset1:112
	s_mov_b64 exec, s[64:65]
	v_mov_b32_e32 v4, 0
	v_lshlrev_b32_e32 v10, 2, v189
	v_mov_b32_e32 v11, v4
	v_and_b32_e32 v70, 0x1c0, v0
	s_waitcnt lgkmcnt(0)
	v_lshl_add_u64 v[2:3], s[44:45], 0, v[10:11]
	s_lshl_b64 s[0:1], s[42:43], 17
	v_lshlrev_b32_e32 v6, 8, v70
	v_mov_b32_e32 v7, v4
	v_lshl_add_u64 v[2:3], v[2:3], 0, s[0:1]
	v_lshl_add_u64 v[2:3], v[2:3], 0, v[6:7]
	s_movk_i32 s0, 0x1000
	v_add_co_u32_e32 v6, vcc, s0, v2
	s_movk_i32 s0, 0x2000
	s_nop 0
	v_addc_co_u32_e32 v7, vcc, 0, v3, vcc
	v_add_co_u32_e32 v8, vcc, s0, v2
	s_movk_i32 s0, 0x3000
	s_nop 0
	v_addc_co_u32_e32 v9, vcc, 0, v3, vcc
	global_load_dword v78, v[2:3], off
	global_load_dword v77, v[2:3], off offset:256
	global_load_dword v76, v[2:3], off offset:512
	global_load_dword v75, v[2:3], off offset:768
	global_load_dword v74, v[2:3], off offset:1024
	global_load_dword v73, v[2:3], off offset:1280
	global_load_dword v72, v[2:3], off offset:1536
	global_load_dword v71, v[2:3], off offset:1792
	global_load_dword v69, v[2:3], off offset:2048
	global_load_dword v65, v[2:3], off offset:2304
	global_load_dword v63, v[2:3], off offset:2560
	global_load_dword v62, v[2:3], off offset:2816
	global_load_dword v61, v[2:3], off offset:3072
	global_load_dword v51, v[2:3], off offset:3328
	global_load_dword v52, v[2:3], off offset:3584
	global_load_dword v53, v[2:3], off offset:3840
	v_add_co_u32_e32 v2, vcc, s0, v2
	global_load_dword v55, v[6:7], off offset:256
	global_load_dword v56, v[6:7], off offset:512
	global_load_dword v57, v[6:7], off offset:768
	global_load_dword v54, v[6:7], off offset:1024
	global_load_dword v48, v[6:7], off offset:1280
	global_load_dword v49, v[6:7], off offset:1536
	global_load_dword v50, v[6:7], off offset:1792
	global_load_dword v47, v[6:7], off offset:2048
	global_load_dword v43, v[8:9], off
	global_load_dword v44, v[8:9], off offset:256
	global_load_dword v45, v[8:9], off offset:512
	global_load_dword v46, v[8:9], off offset:768
	global_load_dword v42, v[8:9], off offset:1024
	global_load_dword v39, v[8:9], off offset:1280
	global_load_dword v40, v[8:9], off offset:1536
	global_load_dword v41, v[8:9], off offset:1792
	global_load_dword v33, v[8:9], off offset:2048
	global_load_dword v34, v[8:9], off offset:2304
	global_load_dword v35, v[8:9], off offset:2560
	global_load_dword v36, v[8:9], off offset:2816
	global_load_dword v32, v[8:9], off offset:3072
	global_load_dword v24, v[8:9], off offset:3328
	global_load_dword v25, v[8:9], off offset:3584
	global_load_dword v26, v[8:9], off offset:3840
	v_addc_co_u32_e32 v3, vcc, 0, v3, vcc
	global_load_dword v66, v[6:7], off offset:2304
	global_load_dword v67, v[6:7], off offset:2560
	global_load_dword v68, v[6:7], off offset:2816
	global_load_dword v64, v[6:7], off offset:3072
	global_load_dword v58, v[6:7], off offset:3328
	global_load_dword v59, v[6:7], off offset:3584
	global_load_dword v60, v[6:7], off offset:3840
	global_load_dword v28, v[2:3], off
	global_load_dword v29, v[2:3], off offset:256
	global_load_dword v30, v[2:3], off offset:512
	global_load_dword v31, v[2:3], off offset:768
	global_load_dword v27, v[2:3], off offset:1024
	global_load_dword v21, v[2:3], off offset:1280
	global_load_dword v22, v[2:3], off offset:1536
	global_load_dword v23, v[2:3], off offset:1792
	global_load_dword v16, v[2:3], off offset:2048
	global_load_dword v79, v[8:9], off offset:-4096
	global_load_dword v18, v[2:3], off offset:2304
	global_load_dword v19, v[2:3], off offset:2560
	global_load_dword v20, v[2:3], off offset:2816
	global_load_dword v17, v[2:3], off offset:3072
	global_load_dword v15, v[2:3], off offset:3328
	global_load_dword v13, v[2:3], off offset:3584
	global_load_dword v11, v[2:3], off offset:3840
	v_lshl_add_u32 v2, v189, 2, 0
	v_add_u32_e32 v5, 0x20000, v2
	s_waitcnt vmcnt(63) expcnt(7) lgkmcnt(15)
	s_barrier
	ds_read2st64_b32 v[2:3], v5 offset1:1
	ds_read2st64_b32 v[6:7], v5 offset0:2 offset1:3
	ds_read2st64_b32 v[8:9], v5 offset0:4 offset1:5
	ds_read2st64_b32 v[80:81], v5 offset0:6 offset1:7
	s_mov_b32 s7, 0
	s_waitcnt lgkmcnt(3)
	v_add_f32_e32 v2, s2, v2
	v_add_f32_e32 v3, s2, v3
	s_waitcnt lgkmcnt(2)
	v_add_f32_e32 v2, v2, v6
	v_add_f32_e32 v3, v3, v7
	s_waitcnt lgkmcnt(1)
	v_add_f32_e32 v2, v2, v8
	v_add_f32_e32 v6, v3, v9
	s_waitcnt lgkmcnt(0)
	v_add_f32_e32 v12, v2, v80
	ds_read2st64_b32 v[2:3], v5 offset0:8 offset1:9
	v_add_f32_e32 v14, v6, v81
	ds_read2st64_b32 v[6:7], v5 offset0:10 offset1:11
	ds_read2st64_b32 v[8:9], v5 offset0:12 offset1:13
	ds_read2st64_b32 v[80:81], v5 offset0:14 offset1:15
	v_cmp_gt_u32_e64 s[0:1], 64, v0
	s_waitcnt lgkmcnt(3)
	v_add_f32_e32 v2, v12, v2
	v_add_f32_e32 v3, v14, v3
	s_waitcnt lgkmcnt(2)
	v_add_f32_e32 v2, v2, v6
	v_add_f32_e32 v3, v3, v7
	s_waitcnt lgkmcnt(1)
	v_add_f32_e32 v2, v2, v8
	v_add_f32_e32 v3, v3, v9
	s_waitcnt lgkmcnt(0)
	v_add_f32_e32 v2, v2, v80
	v_add_f32_e32 v3, v3, v81
	v_max_f32_e32 v5, v2, v3
	s_nop 1
	v_max_f32_dpp v5, v5, v5 quad_perm:[1,0,3,2] row_mask:0xf bank_mask:0xf
	s_nop 1
	v_max_f32_dpp v5, v5, v5 quad_perm:[2,3,0,1] row_mask:0xf bank_mask:0xf
	s_nop 1
	v_max_f32_dpp v5, v5, v5 row_half_mirror row_mask:0xf bank_mask:0xf
	s_nop 1
	v_max_f32_dpp v5, v5, v5 row_mirror row_mask:0xf bank_mask:0xf
	ds_bpermute_b32 v6, v181, v5
	s_waitcnt lgkmcnt(0)
	v_max_f32_e32 v5, v5, v6
	ds_bpermute_b32 v6, v183, v5
	s_waitcnt lgkmcnt(0)
	v_max_f32_e32 v14, v5, v6
	v_sub_f32_e32 v2, v2, v14
	v_sub_f32_e32 v3, v3, v14
	v_mul_f32_e32 v2, 0x3fb8aa3b, v2
	v_mul_f32_e32 v3, 0x3fb8aa3b, v3
	v_exp_f32_e32 v2, v2
	v_exp_f32_e32 v3, v3
	s_nop 0
	v_add_f32_e32 v5, v2, v3
	s_nop 1
	v_add_f32_dpp v5, v5, v5 quad_perm:[1,0,3,2] row_mask:0xf bank_mask:0xf
	s_nop 1
	v_add_f32_dpp v5, v5, v5 quad_perm:[2,3,0,1] row_mask:0xf bank_mask:0xf
	s_nop 1
	v_add_f32_dpp v5, v5, v5 row_half_mirror row_mask:0xf bank_mask:0xf
	s_nop 1
	v_add_f32_dpp v5, v5, v5 row_mirror row_mask:0xf bank_mask:0xf
	ds_bpermute_b32 v6, v181, v5
	s_waitcnt lgkmcnt(0)
	v_add_f32_e32 v37, v5, v6
	ds_bpermute_b32 v38, v183, v37
	s_and_saveexec_b64 s[2:3], s[0:1]
	s_cbranch_execz .LBB5_166
	s_add_i32 s12, 0, 0x21000
	v_lshl_add_u32 v5, v189, 2, s12
	v_lshl_add_u32 v6, v0, 2, s12
	ds_write_b32 v5, v2
	ds_write_b32 v6, v3 offset:256

	.amdhsa_kernel _Z8k_expertPKDF16_S0_PKfPcPiS0_S2_S2_S2_S2_PfS5_S4_S2_S2_S2_S2_S5_S2_S2_S2_
		.amdhsa_group_segment_fixed_size 0
		.amdhsa_private_segment_fixed_size 0
		.amdhsa_kernarg_size 168
		.amdhsa_user_sgpr_count 2
		.amdhsa_user_sgpr_dispatch_ptr 0
		.amdhsa_user_sgpr_queue_ptr 0
		.amdhsa_user_sgpr_kernarg_segment_ptr 1
		.amdhsa_user_sgpr_dispatch_id 0
		.amdhsa_user_sgpr_kernarg_preload_length 0
		.amdhsa_user_sgpr_kernarg_preload_offset 0
		.amdhsa_user_sgpr_private_segment_size 0
		.amdhsa_uses_dynamic_stack 0
		.amdhsa_enable_private_segment 0
		.amdhsa_system_sgpr_workgroup_id_x 1
		.amdhsa_system_sgpr_workgroup_id_y 0
		.amdhsa_system_sgpr_workgroup_id_z 0
		.amdhsa_system_sgpr_workgroup_info 0
		.amdhsa_system_vgpr_workitem_id 0
		.amdhsa_next_free_vgpr 256
		.amdhsa_next_free_sgpr 100
		.amdhsa_accum_offset 256
		.amdhsa_reserve_vcc 1
		.amdhsa_float_round_mode_32 0
		.amdhsa_float_round_mode_16_64 0
		.amdhsa_float_denorm_mode_32 3
		.amdhsa_float_denorm_mode_16_64 3
		.amdhsa_dx10_clamp 1
		.amdhsa_ieee_mode 1
		.amdhsa_fp16_overflow 0
		.amdhsa_tg_split 0
		.amdhsa_exception_fp_ieee_invalid_op 0
		.amdhsa_exception_fp_denorm_src 0
		.amdhsa_exception_fp_ieee_div_zero 0
		.amdhsa_exception_fp_ieee_overflow 0
		.amdhsa_exception_fp_ieee_underflow 0
		.amdhsa_exception_fp_ieee_inexact 0
		.amdhsa_exception_int_div_zero 0
	.end_amdhsa_kernel

amdhsa.kernels:
  - .agpr_count:     0
    .args:
      - .actual_access:  read_only
        .address_space:  global
        .offset:         0
        .size:           8
        .value_kind:     global_buffer
      - .actual_access:  read_only
        .address_space:  global
        .offset:         8
        .size:           8
        .value_kind:     global_buffer
      - .actual_access:  read_only
        .address_space:  global
        .offset:         16
        .size:           8
        .value_kind:     global_buffer
      - .actual_access:  write_only
        .address_space:  global
        .offset:         24
        .size:           8
        .value_kind:     global_buffer
      - .actual_access:  write_only
        .address_space:  global
        .offset:         32
        .size:           8
        .value_kind:     global_buffer
      - .actual_access:  read_only
        .address_space:  global
        .offset:         40
        .size:           8
        .value_kind:     global_buffer
      - .actual_access:  read_only
        .address_space:  global
        .offset:         48
        .size:           8
        .value_kind:     global_buffer
      - .actual_access:  read_only
        .address_space:  global
        .offset:         56
        .size:           8
        .value_kind:     global_buffer
      - .actual_access:  read_only
        .address_space:  global
        .offset:         64
        .size:           8
        .value_kind:     global_buffer
      - .actual_access:  read_only
        .address_space:  global
        .offset:         72
        .size:           8
        .value_kind:     global_buffer
      - .actual_access:  read_only
        .address_space:  global
        .offset:         80
        .size:           8
        .value_kind:     global_buffer
    .group_segment_fixed_size: 16384
    .kernarg_segment_align: 8
    .kernarg_segment_size: 88
    .language:       OpenCL C
    .language_version:
      - 2
      - 0
    .max_flat_workgroup_size: 768
    .name:           _Z9k_router2PKfPKDF16_S0_PDF16_PfPiS0_S0_S4_S5_S4_
    .private_segment_fixed_size: 0
    .sgpr_count:     21
    .sgpr_spill_count: 0
    .symbol:         _Z9k_router2PKfPKDF16_S0_PDF16_PfPiS0_S0_S4_S5_S4_.kd
    .uniform_work_group_size: 1
    .uses_dynamic_stack: false
    .vgpr_count:     168
    .vgpr_spill_count: 0
    .wavefront_size: 64
  - .agpr_count:     0
    .args:
      - .actual_access:  read_only
        .address_space:  global
        .offset:         0
        .size:           8
        .value_kind:     global_buffer
      - .actual_access:  read_only
        .address_space:  global
        .offset:         8
        .size:           8
        .value_kind:     global_buffer
      - .actual_access:  read_only
        .address_space:  global
        .offset:         16
        .size:           8
        .value_kind:     global_buffer
      - .actual_access:  write_only
        .address_space:  global
        .offset:         24
        .size:           8
        .value_kind:     global_buffer
      - .actual_access:  write_only
        .address_space:  global
        .offset:         32
        .size:           8
        .value_kind:     global_buffer
      - .actual_access:  write_only
        .address_space:  global
        .offset:         40
        .size:           8
        .value_kind:     global_buffer
    .group_segment_fixed_size: 256
    .kernarg_segment_align: 8
    .kernarg_segment_size: 48
    .language:       OpenCL C
    .language_version:
      - 2
      - 0
    .max_flat_workgroup_size: 256
    .name:           _Z6k_gatePKfS0_S0_PfPiS1_
    .private_segment_fixed_size: 0
    .sgpr_count:     26
    .sgpr_spill_count: 0
    .symbol:         _Z6k_gatePKfS0_S0_PfPiS1_.kd
    .uniform_work_group_size: 1
    .uses_dynamic_stack: false
    .vgpr_count:     51
    .vgpr_spill_count: 0
    .wavefront_size: 64
  - .agpr_count:     0
    .args:
      - .actual_access:  read_only
        .address_space:  global
        .offset:         0
        .size:           8
        .value_kind:     global_buffer
      - .actual_access:  write_only
        .address_space:  global
        .offset:         8
        .size:           8
        .value_kind:     global_buffer
      - .actual_access:  read_only
        .address_space:  global
        .offset:         16
        .size:           8
        .value_kind:     global_buffer
      - .actual_access:  read_only
        .address_space:  global
        .offset:         24
        .size:           8
        .value_kind:     global_buffer
      - .actual_access:  read_only
        .address_space:  global
        .offset:         32
        .size:           8
        .value_kind:     global_buffer
      - .actual_access:  write_only
        .address_space:  global
        .offset:         40
        .size:           8
        .value_kind:     global_buffer
      - .actual_access:  write_only
        .address_space:  global
        .offset:         48
        .size:           8
        .value_kind:     global_buffer
      - .actual_access:  write_only
        .address_space:  global
        .offset:         56
        .size:           8
        .value_kind:     global_buffer
      - .actual_access:  write_only
        .address_space:  global
        .offset:         64
        .size:           8
        .value_kind:     global_buffer
      - .actual_access:  write_only
        .address_space:  global
        .offset:         72
        .size:           8
        .value_kind:     global_buffer
    .group_segment_fixed_size: 16640
    .kernarg_segment_align: 8
    .kernarg_segment_size: 80
    .language:       OpenCL C
    .language_version:
      - 2
      - 0
    .max_flat_workgroup_size: 256
    .name:           _Z10k_prep_allPKfPDF16_S0_S0_S0_S1_S1_PiS2_S2_
    .private_segment_fixed_size: 0
    .sgpr_count:     20
    .sgpr_spill_count: 0
    .symbol:         _Z10k_prep_allPKfPDF16_S0_S0_S0_S1_S1_PiS2_S2_.kd
    .uniform_work_group_size: 1
    .uses_dynamic_stack: false
    .vgpr_count:     37
    .vgpr_spill_count: 0
    .wavefront_size: 64
  - .agpr_count:     0
    .args:
      - .address_space:  global
        .offset:         0
        .size:           8
        .value_kind:     global_buffer
      - .address_space:  global
        .offset:         8
        .size:           8
        .value_kind:     global_buffer
      - .actual_access:  read_only
        .address_space:  global
        .offset:         16
        .size:           8
        .value_kind:     global_buffer
      - .actual_access:  read_only
        .address_space:  global
        .offset:         24
        .size:           8
        .value_kind:     global_buffer
      - .actual_access:  write_only
        .address_space:  global
        .offset:         32
        .size:           8
        .value_kind:     global_buffer
    .group_segment_fixed_size: 0
    .kernarg_segment_align: 8
    .kernarg_segment_size: 40
    .language:       OpenCL C
    .language_version:
      - 2
      - 0
    .max_flat_workgroup_size: 512
    .name:           _Z7k_gemm1PKDF16_S0_PKfPKiPDF16_
    .private_segment_fixed_size: 0
    .sgpr_count:     36
    .sgpr_spill_count: 0
    .symbol:         _Z7k_gemm1PKDF16_S0_PKfPKiPDF16_.kd
    .uniform_work_group_size: 1
    .uses_dynamic_stack: false
    .vgpr_count:     240
    .vgpr_spill_count: 0
    .wavefront_size: 64
  - .agpr_count:     0
    .args:
      - .address_space:  global
        .offset:         0
        .size:           8
        .value_kind:     global_buffer
      - .actual_access:  read_only
        .address_space:  global
        .offset:         8
        .size:           8
        .value_kind:     global_buffer
      - .actual_access:  read_only
        .address_space:  global
        .offset:         16
        .size:           8
        .value_kind:     global_buffer
      - .actual_access:  read_only
        .address_space:  global
        .offset:         24
        .size:           8
        .value_kind:     global_buffer
      - .actual_access:  read_only
        .address_space:  global
        .offset:         32
        .size:           8
        .value_kind:     global_buffer
      - .actual_access:  read_only
        .address_space:  global
        .offset:         40
        .size:           8
        .value_kind:     global_buffer
      - .actual_access:  read_only
        .address_space:  global
        .offset:         48
        .size:           8
        .value_kind:     global_buffer
      - .actual_access:  write_only
        .address_space:  global
        .offset:         56
        .size:           8
        .value_kind:     global_buffer
      - .actual_access:  write_only
        .address_space:  global
        .offset:         64
        .size:           8
        .value_kind:     global_buffer
    .group_segment_fixed_size: 0
    .kernarg_segment_align: 8
    .kernarg_segment_size: 72
    .language:       OpenCL C
    .language_version:
      - 2
      - 0
    .max_flat_workgroup_size: 512
    .name:           _Z11k_gemm2poolPKDF16_S0_PKfS2_S2_S2_PKiPfS5_
    .private_segment_fixed_size: 0
    .sgpr_count:     32
    .sgpr_spill_count: 0
    .symbol:         _Z11k_gemm2poolPKDF16_S0_PKfS2_S2_S2_PKiPfS5_.kd
    .uniform_work_group_size: 1
    .uses_dynamic_stack: false
    .vgpr_count:     198
    .vgpr_spill_count: 0
    .wavefront_size: 64
  - .agpr_count:     0
    .args:
      - .address_space:  global
        .offset:         0
        .size:           8
        .value_kind:     global_buffer
      - .address_space:  global
        .offset:         8
        .size:           8
        .value_kind:     global_buffer
      - .actual_access:  read_only
        .address_space:  global
        .offset:         16
        .size:           8
        .value_kind:     global_buffer
      - .address_space:  global
        .offset:         24
        .size:           8
        .value_kind:     global_buffer
      - .address_space:  global
        .offset:         32
        .size:           8
        .value_kind:     global_buffer
      - .actual_access:  read_only
        .address_space:  global
        .offset:         40
        .size:           8
        .value_kind:     global_buffer
      - .actual_access:  read_only
        .address_space:  global
        .offset:         48
        .size:           8
        .value_kind:     global_buffer
      - .actual_access:  read_only
        .address_space:  global
        .offset:         56
        .size:           8
        .value_kind:     global_buffer
      - .actual_access:  read_only
        .address_space:  global
        .offset:         64
        .size:           8
        .value_kind:     global_buffer
      - .actual_access:  read_only
        .address_space:  global
        .offset:         72
        .size:           8
        .value_kind:     global_buffer
      - .address_space:  global
        .offset:         80
        .size:           8
        .value_kind:     global_buffer
      - .address_space:  global
        .offset:         88
        .size:           8
        .value_kind:     global_buffer
      - .address_space:  global
        .offset:         96
        .size:           8
        .value_kind:     global_buffer
      - .actual_access:  read_only
        .address_space:  global
        .offset:         104
        .size:           8
        .value_kind:     global_buffer
      - .actual_access:  read_only
        .address_space:  global
        .offset:         112
        .size:           8
        .value_kind:     global_buffer
      - .actual_access:  read_only
        .address_space:  global
        .offset:         120
        .size:           8
        .value_kind:     global_buffer
      - .actual_access:  read_only
        .address_space:  global
        .offset:         128
        .size:           8
        .value_kind:     global_buffer
      - .actual_access:  write_only
        .address_space:  global
        .offset:         136
        .size:           8
        .value_kind:     global_buffer
      - .actual_access:  read_only
        .address_space:  global
        .offset:         144
        .size:           8
        .value_kind:     global_buffer
      - .actual_access:  read_only
        .address_space:  global
        .offset:         152
        .size:           8
        .value_kind:     global_buffer
      - .actual_access:  read_only
        .address_space:  global
        .offset:         160
        .size:           8
        .value_kind:     global_buffer
    .group_segment_fixed_size: 0
    .kernarg_segment_align: 8
    .kernarg_segment_size: 168
    .language:       OpenCL C
    .language_version:
      - 2
      - 0
    .max_flat_workgroup_size: 512
    .name:           _Z8k_expertPKDF16_S0_PKfPcPiS0_S2_S2_S2_S2_PfS5_S4_S2_S2_S2_S2_S5_S2_S2_S2_
    .private_segment_fixed_size: 0
    .sgpr_count:     106
    .sgpr_spill_count: 0
    .symbol:         _Z8k_expertPKDF16_S0_PKfPcPiS0_S2_S2_S2_S2_PfS5_S4_S2_S2_S2_S2_S5_S2_S2_S2_.kd
    .uniform_work_group_size: 1
    .uses_dynamic_stack: false
    .vgpr_count:     256
    .vgpr_spill_count: 0
    .wavefront_size: 64
  - .agpr_count:     0
    .args:
      - .actual_access:  read_only
        .address_space:  global
        .offset:         0
        .size:           8
        .value_kind:     global_buffer
      - .actual_access:  read_only
        .address_space:  global
        .offset:         8
        .size:           8
        .value_kind:     global_buffer
      - .actual_access:  read_only
        .address_space:  global
        .offset:         16
        .size:           8
        .value_kind:     global_buffer
      - .actual_access:  read_only
        .address_space:  global
        .offset:         24
        .size:           8
        .value_kind:     global_buffer
      - .actual_access:  read_only
        .address_space:  global
        .offset:         32
        .size:           8
        .value_kind:     global_buffer
      - .actual_access:  read_only
        .address_space:  global
        .offset:         40
        .size:           8
        .value_kind:     global_buffer
      - .actual_access:  read_only
        .address_space:  global
        .offset:         48
        .size:           8
        .value_kind:     global_buffer
      - .actual_access:  read_only
        .address_space:  global
        .offset:         56
        .size:           8
        .value_kind:     global_buffer
      - .actual_access:  write_only
        .address_space:  global
        .offset:         64
        .size:           8
        .value_kind:     global_buffer
    .group_segment_fixed_size: 8768
    .kernarg_segment_align: 8
    .kernarg_segment_size: 72
    .language:       OpenCL C
    .language_version:
      - 2
      - 0
    .max_flat_workgroup_size: 1024
    .name:           _Z7k_finalPKfS0_S0_S0_S0_PKiS0_S0_Pf
    .private_segment_fixed_size: 0
    .sgpr_count:     24
    .sgpr_spill_count: 0
    .symbol:         _Z7k_finalPKfS0_S0_S0_S0_PKiS0_S0_Pf.kd
    .uniform_work_group_size: 1
    .uses_dynamic_stack: false
    .vgpr_count:     83
    .vgpr_spill_count: 0
    .wavefront_size: 64
